# v90 + non-temporal hint on the MoE down-projection output (y) stores
# baseline (speedup 1.0000x reference)
.LBB0_906:
	s_waitcnt lgkmcnt(0)
	v_mov_b32_e32 v52, v244
	v_mov_b32_e32 v53, 0
	s_waitcnt vmcnt(7)
	v_cvt_pk_bf16_f32 v4, v4, v5
	v_mbcnt_lo_u32_b32 v53, -1, v53
	v_mbcnt_hi_u32_b32 v53, -1, v53
	s_waitcnt lgkmcnt(0)
	v_readfirstlane_b32 s6, v52
	v_cvt_pk_bf16_f32 v5, v6, v7
	s_waitcnt vmcnt(6)
	v_cvt_pk_bf16_f32 v0, v0, v1
	v_lshl_or_b32 v62, s6, 6, v53
	v_cvt_pk_bf16_f32 v1, v2, v3
	v_lshrrev_b32_e32 v53, 3, v62
	v_lshlrev_b32_e32 v54, 4, v62
	v_and_b32_e32 v68, 0x70, v54
	v_mul_lo_u32 v69, v53, s20
	v_ashrrev_i32_e32 v52, 5, v62
	v_add3_u32 v53, 0, v68, v69
	ds_write_b128 v53, v[32:35]
	ds_write_b128 v53, v[36:39] offset:9216
	ds_write_b128 v53, v[40:43] offset:18432
	s_waitcnt vmcnt(5)
	ds_write_b128 v53, v[44:47] offset:27648
	s_waitcnt vmcnt(4)
	ds_write_b128 v53, v[48:51] offset:36864
	v_lshrrev_b32_e32 v34, 1, v52
	v_bfe_u32 v32, v62, 2, 3
	v_and_b32_e32 v33, 3, v52
	v_and_b32_e32 v34, 4, v34
	v_bitop3_b32 v32, v34, v32, v33 bitop3:0x36
	v_lshlrev_b32_e32 v33, 2, v62
	v_and_b32_e32 v67, 12, v33
	v_lshlrev_b32_e32 v70, 1, v67
	v_lshl_or_b32 v130, v32, 5, v70
	v_lshlrev_b32_e32 v131, 8, v52
	v_add3_u32 v6, s21, v130, v131
	ds_write2st64_b64 v6, v[4:5], v[0:1] offset1:8
	s_waitcnt vmcnt(5)
	v_cvt_pk_bf16_f32 v0, v12, v13
	v_cvt_pk_bf16_f32 v1, v14, v15
	s_waitcnt vmcnt(4)
	v_cvt_pk_bf16_f32 v2, v8, v9
	v_cvt_pk_bf16_f32 v3, v10, v11
	ds_write2st64_b64 v6, v[0:1], v[2:3] offset0:16 offset1:24
	v_sub_u32_e32 v0, v156, v143
	v_xad_u32 v2, s14, -1, v0
	v_add_u32_e32 v1, s14, v141
	v_min_i32_e32 v0, 0, v2
	v_add_u32_e32 v3, v1, v143
	v_add_u32_e32 v0, v0, v3
	v_ashrrev_i32_e32 v1, 31, v0
	v_lshlrev_b64 v[0:1], 9, v[0:1]
	v_lshl_add_u64 v[52:53], v[134:135], 0, v[0:1]
	v_min_i32_e32 v0, 64, v2
	v_add_u32_e32 v0, v0, v3
	v_ashrrev_i32_e32 v1, 31, v0
	v_lshlrev_b64 v[0:1], 9, v[0:1]
	v_lshl_add_u64 v[54:55], v[134:135], 0, v[0:1]
	v_min_i32_e32 v0, 0x80, v2
	v_add_u32_e32 v0, v0, v3
	v_ashrrev_i32_e32 v1, 31, v0
	v_lshlrev_b64 v[0:1], 9, v[0:1]
	v_lshl_add_u64 v[56:57], v[134:135], 0, v[0:1]
	v_min_i32_e32 v0, 0xc0, v2
	v_add_u32_e32 v0, v0, v3
	v_ashrrev_i32_e32 v1, 31, v0
	v_lshlrev_b64 v[0:1], 9, v[0:1]
	v_lshl_add_u64 v[58:59], v[134:135], 0, v[0:1]
	v_min_i32_e32 v0, 0x100, v2
	v_add_u32_e32 v0, v0, v3
	v_ashrrev_i32_e32 v1, 31, v0
	v_lshlrev_b64 v[0:1], 9, v[0:1]
	v_lshl_add_u64 v[60:61], v[134:135], 0, v[0:1]
	v_lshrrev_b32_e32 v1, 2, v62
	v_bfe_u32 v65, v62, 2, 2
	v_and_b32_e32 v1, 4, v1
	v_bfe_u32 v66, v62, 6, 1
	v_lshrrev_b32_e32 v0, 1, v62
	v_or_b32_e32 v2, v1, v65
	v_and_b32_e32 v71, 24, v0
	v_lshlrev_b32_e32 v3, 6, v66
	v_lshlrev_b32_e32 v2, 4, v2
	s_cmpk_lt_i32 s13, 0x100
	v_readlane_b32 s44, v253, 4
	v_or_b32_e32 v0, v71, v65
	v_xor_b32_e32 v2, v2, v3
	s_cselect_b32 s6, s13, 0
	v_readlane_b32 s50, v253, 10
	v_readlane_b32 s51, v253, 11
	v_readlane_b32 s56, v253, 16
	v_readlane_b32 s57, v253, 17
	v_or_b32_e32 v2, v2, v67
	v_lshlrev_b32_e32 v72, 8, v0
	v_lshlrev_b32_e32 v0, 2, v66
	s_cselect_b32 s9, s51, s57
	s_cselect_b32 s8, s50, s56
	s_ashr_i32 s7, s6, 31
	v_lshlrev_b32_e32 v192, 1, v2
	v_or_b32_e32 v2, 1, v0
	s_lshl_b64 s[6:7], s[6:7], 20
	v_bitop3_b32 v2, v1, v2, v65 bitop3:0x36
	s_add_u32 s8, s8, s6
	v_lshl_or_b32 v196, v2, 5, v70
	v_or_b32_e32 v2, 2, v0
	v_or_b32_e32 v0, 3, v0
	s_addc_u32 s9, s9, s7
	s_lshl_b32 s6, s15, 7
	v_bitop3_b32 v0, v1, v0, v65 bitop3:0x36
	s_ashr_i32 s7, s6, 31
	v_bitop3_b32 v2, v1, v2, v65 bitop3:0x36
	v_lshl_or_b32 v200, v0, 5, v70
	v_lshl_add_u64 v[0:1], s[8:9], 0, v[144:145]
	s_lshl_b64 s[10:11], s[6:7], 2
	v_lshl_add_u64 v[0:1], v[0:1], 0, s[10:11]
	v_lshl_add_u64 v[0:1], v[0:1], 0, v[132:133]
	v_mov_b32_e32 v149, v133
	v_lshl_add_u64 v[0:1], v[0:1], 0, v[148:149]
	v_mov_b32_e32 v151, v133
	v_lshl_add_u64 v[0:1], v[0:1], 0, v[150:151]
	v_lshl_or_b32 v197, v2, 5, v70
	v_add_co_u32_e32 v2, vcc, s16, v0
	global_load_dwordx4 v[32:35], v[52:53], off offset:128
	global_load_dwordx4 v[36:39], v[54:55], off offset:128
	v_addc_co_u32_e32 v3, vcc, 0, v1, vcc
	global_load_dwordx4 v[40:43], v[56:57], off offset:128
	global_load_dwordx4 v[44:47], v[58:59], off offset:128
	global_load_dwordx4 v[48:51], v[60:61], off offset:128
	s_waitcnt lgkmcnt(0)
	s_barrier
	global_load_dwordx4 v[12:15], v[0:1], off
	global_load_dwordx4 v[8:11], v[2:3], off
	v_add_co_u32_e32 v2, vcc, s17, v0
	v_ashrrev_i32_e32 v63, 7, v62
	s_nop 0
	v_addc_co_u32_e32 v3, vcc, 0, v1, vcc
	v_add_co_u32_e32 v0, vcc, s18, v0
	v_and_b32_e32 v64, 15, v62
	s_nop 0
	v_addc_co_u32_e32 v1, vcc, 0, v1, vcc
	global_load_dwordx4 v[4:7], v[2:3], off
	s_nop 0
	global_load_dwordx4 v[0:3], v[0:1], off
	v_add_u32_e32 v62, s21, v72
	v_add_u32_e32 v81, v62, v192
	v_add_u32_e32 v83, v62, v196
	v_add_u32_e32 v79, v62, v197
	v_add_u32_e32 v100, v62, v200
	v_mul_lo_u32 v62, v63, s19
	v_add_u32_e32 v193, 0, v72
	v_or_b32_e32 v62, v62, v64
	v_add_u32_e32 v67, 0x16c00, v193
	v_lshlrev_b32_e32 v63, 1, v71
	v_mul_lo_u32 v62, v62, s20
	v_add_u32_e32 v82, v67, v192
	v_add_u32_e32 v84, v67, v196
	v_add_u32_e32 v80, v67, v197
	v_add_u32_e32 v101, v67, v200
	v_add3_u32 v62, 0, v63, v62
	ds_read_b64_tr_b16 v[102:103], v81
	ds_read_b64_tr_b16 v[104:105], v82
	ds_read_b64_tr_b16 v[106:107], v83
	ds_read_b64_tr_b16 v[108:109], v84
	ds_read_b128 v[64:67], v62
	ds_read_b64_tr_b16 v[110:111], v79
	ds_read_b64_tr_b16 v[112:113], v80
	ds_read_b128 v[114:117], v62 offset:2304
	ds_read_b64_tr_b16 v[122:123], v100
	ds_read_b64_tr_b16 v[124:125], v101
	s_waitcnt lgkmcnt(5)
	v_mfma_f32_16x16x32_bf16 v[118:121], v[102:105], v[64:67], 0
	v_add3_u32 v63, 0, v131, v130
	v_or_b32_e32 v201, 0x2000, v72
	v_add_u32_e32 v70, 0x18c00, v193
	v_mfma_f32_16x16x32_bf16 v[126:129], v[106:109], v[64:67], 0
	v_add3_u32 v86, 0, v69, v68
	v_add_u32_e32 v68, s22, v72
	ds_read_b128 v[180:183], v62 offset:4608
	ds_read_b128 v[184:187], v62 offset:6912
	s_waitcnt lgkmcnt(5)
	v_mfma_f32_16x16x32_bf16 v[152:155], v[110:113], v[64:67], 0
	v_add_u32_e32 v98, 0x1b800, v63
	v_add_u32_e32 v95, 0x1c800, v63
	v_add_u32_e32 v92, 0x1d800, v63
	s_waitcnt lgkmcnt(2)
	v_mfma_f32_16x16x32_bf16 v[164:167], v[122:125], v[64:67], 0
	v_add_u32_e32 v64, 0x1ac00, v193
	v_add_u32_e32 v78, v64, v192
	v_add_u32_e32 v75, v64, v196
	v_add_u32_e32 v73, v64, v197
	v_add_u32_e32 v72, v64, v200
	v_add_u32_e32 v64, 0x1cc00, v193
	v_add3_u32 v91, s21, v192, v201
	v_add_u32_e32 v93, v70, v192
	v_add3_u32 v89, s21, v196, v201
	v_add_u32_e32 v90, v70, v196
	v_add3_u32 v85, s21, v197, v201
	v_add_u32_e32 v94, v70, v197
	v_add3_u32 v96, s21, v200, v201
	v_add_u32_e32 v97, v70, v200
	v_add_u32_e32 v77, v68, v192
	v_add_u32_e32 v74, v68, v196
	v_mfma_f32_16x16x32_bf16 v[168:171], v[102:105], v[114:117], 0
	v_add_u32_e32 v76, v68, v197
	v_add_u32_e32 v71, v68, v200
	v_add_u32_e32 v241, 0x17800, v63
	v_mfma_f32_16x16x32_bf16 v[172:175], v[106:109], v[114:117], 0
	v_add_u32_e32 v242, 0x18800, v63
	v_add_u32_e32 v243, 0x19800, v63
	v_add3_u32 v68, s22, v192, v201
	v_mfma_f32_16x16x32_bf16 v[176:179], v[110:113], v[114:117], 0
	v_add_u32_e32 v70, v64, v192
	v_add3_u32 v67, s22, v196, v201
	v_add_u32_e32 v69, v64, v196
	v_mfma_f32_16x16x32_bf16 v[114:117], v[122:125], v[114:117], 0
	v_add3_u32 v65, s22, v197, v201
	v_add_u32_e32 v66, v64, v197
	v_add3_u32 v63, s22, v200, v201
	v_add_u32_e32 v64, v64, v200
	ds_read_b128 v[200:203], v62 offset:9216
	v_add3_u32 v99, s22, v131, v130
	v_add_u32_e32 v87, 0x12000, v86
	v_add_u32_e32 v88, 0x14400, v86
	s_waitcnt vmcnt(12)
	v_cvt_pk_bf16_f32 v28, v28, v29
	v_cvt_pk_bf16_f32 v29, v30, v31
	s_waitcnt vmcnt(11)
	v_cvt_pk_bf16_f32 v24, v24, v25
	v_cvt_pk_bf16_f32 v25, v26, v27
	v_readlane_b32 s45, v253, 5
	v_readlane_b32 s46, v253, 6
	v_readlane_b32 s47, v253, 7
	v_readlane_b32 s48, v253, 8
	v_readlane_b32 s49, v253, 9
	v_readlane_b32 s52, v253, 12
	v_readlane_b32 s53, v253, 13
	v_readlane_b32 s54, v253, 14
	v_readlane_b32 s55, v253, 15
	v_readlane_b32 s58, v253, 18
	v_readlane_b32 s59, v253, 19
	v_add3_u32 v240, s21, v131, v130
	s_waitcnt lgkmcnt(2)
	v_mfma_f32_16x16x32_bf16 v[188:191], v[102:105], v[180:183], 0
	ds_write_b64 v99, v[28:29]
	ds_write_b64 v98, v[24:25]
	v_mfma_f32_16x16x32_bf16 v[192:195], v[106:109], v[180:183], 0
	v_mfma_f32_16x16x32_bf16 v[196:199], v[110:113], v[180:183], 0
	v_mfma_f32_16x16x32_bf16 v[180:183], v[122:125], v[180:183], 0
	ds_read_b128 v[208:211], v62 offset:64
	ds_read_b128 v[212:215], v62 offset:2368
	s_waitcnt vmcnt(9)
	v_cvt_pk_bf16_f32 v16, v16, v17
	v_cvt_pk_bf16_f32 v17, v18, v19
	s_waitcnt lgkmcnt(5)
	v_mfma_f32_16x16x32_bf16 v[24:27], v[102:105], v[184:187], 0
	ds_read_b128 v[216:219], v62 offset:4672
	v_cvt_pk_bf16_f32 v130, v20, v21
	v_cvt_pk_bf16_f32 v131, v22, v23
	v_mfma_f32_16x16x32_bf16 v[28:31], v[106:109], v[184:187], 0
	ds_write_b64 v92, v[16:17]
	ds_write_b64 v95, v[130:131]
	s_waitcnt lgkmcnt(7)
	v_mfma_f32_16x16x32_bf16 v[102:105], v[102:105], v[200:203], 0
	v_mfma_f32_16x16x32_bf16 v[106:109], v[106:109], v[200:203], 0
	v_mfma_f32_16x16x32_bf16 v[20:23], v[110:113], v[200:203], 0
	v_mfma_f32_16x16x32_bf16 v[16:19], v[122:125], v[200:203], 0
	v_mfma_f32_16x16x32_bf16 v[204:207], v[110:113], v[184:187], 0
	v_mfma_f32_16x16x32_bf16 v[184:187], v[122:125], v[184:187], 0
	ds_read_b64_tr_b16 v[110:111], v91
	ds_read_b64_tr_b16 v[112:113], v93
	ds_read_b64_tr_b16 v[122:123], v89
	ds_read_b64_tr_b16 v[124:125], v90
	ds_read_b64_tr_b16 v[200:201], v85
	ds_read_b64_tr_b16 v[202:203], v94
	ds_read_b64_tr_b16 v[220:221], v96
	ds_read_b64_tr_b16 v[222:223], v97
	s_waitcnt lgkmcnt(6)
	v_mfma_f32_16x16x32_bf16 v[118:121], v[110:113], v[208:211], v[118:121]
	s_waitcnt lgkmcnt(4)
	v_mfma_f32_16x16x32_bf16 v[126:129], v[122:125], v[208:211], v[126:129]
	s_waitcnt lgkmcnt(2)
	v_mfma_f32_16x16x32_bf16 v[152:155], v[200:203], v[208:211], v[152:155]
	s_waitcnt lgkmcnt(0)
	v_mfma_f32_16x16x32_bf16 v[164:167], v[220:223], v[208:211], v[164:167]
	v_mfma_f32_16x16x32_bf16 v[168:171], v[110:113], v[212:215], v[168:171]
	v_mfma_f32_16x16x32_bf16 v[172:175], v[122:125], v[212:215], v[172:175]
	v_mfma_f32_16x16x32_bf16 v[176:179], v[200:203], v[212:215], v[176:179]
	v_mfma_f32_16x16x32_bf16 v[114:117], v[220:223], v[212:215], v[114:117]
	ds_read_b128 v[208:211], v62 offset:6976
	ds_read_b128 v[212:215], v62 offset:9280
	s_waitcnt vmcnt(8)
	ds_write_b128 v86, v[32:35] offset:46080
	s_waitcnt vmcnt(7)
	ds_write_b128 v86, v[36:39] offset:55296
	v_mfma_f32_16x16x32_bf16 v[32:35], v[220:223], v[216:219], v[180:183]
	v_mfma_f32_16x16x32_bf16 v[188:191], v[110:113], v[216:219], v[188:191]
	v_mfma_f32_16x16x32_bf16 v[192:195], v[122:125], v[216:219], v[192:195]
	v_mfma_f32_16x16x32_bf16 v[196:199], v[200:203], v[216:219], v[196:199]
	s_waitcnt vmcnt(6)
	ds_write_b128 v86, v[40:43] offset:64512
	s_waitcnt vmcnt(5)
	ds_write_b128 v87, v[44:47]
	s_waitcnt vmcnt(4)
	ds_write_b128 v88, v[48:51]
	s_waitcnt lgkmcnt(6)
	v_mfma_f32_16x16x32_bf16 v[36:39], v[110:113], v[208:211], v[24:27]
	v_mfma_f32_16x16x32_bf16 v[180:183], v[122:125], v[208:211], v[28:31]
	v_mfma_f32_16x16x32_bf16 v[204:207], v[200:203], v[208:211], v[204:207]
	v_mfma_f32_16x16x32_bf16 v[184:187], v[220:223], v[208:211], v[184:187]
	s_waitcnt lgkmcnt(5)
	v_mfma_f32_16x16x32_bf16 v[102:105], v[110:113], v[212:215], v[102:105]
	v_mfma_f32_16x16x32_bf16 v[110:113], v[200:203], v[212:215], v[20:23]
	global_load_dwordx4 v[40:43], v[52:53], off offset:256
	global_load_dwordx4 v[44:47], v[54:55], off offset:256
	global_load_dwordx4 v[48:51], v[56:57], off offset:256
	global_load_dwordx4 v[200:203], v[58:59], off offset:256
	global_load_dwordx4 v[208:211], v[60:61], off offset:256
	v_mfma_f32_16x16x32_bf16 v[106:109], v[122:125], v[212:215], v[106:109]
	v_mfma_f32_16x16x32_bf16 v[122:125], v[220:223], v[212:215], v[16:19]
	s_waitcnt lgkmcnt(0)
	s_barrier
	ds_read_b64_tr_b16 v[212:213], v77
	ds_read_b64_tr_b16 v[214:215], v78
	ds_read_b128 v[16:19], v62 offset:46080
	ds_read_b64_tr_b16 v[216:217], v74
	ds_read_b64_tr_b16 v[218:219], v75
	ds_read_b64_tr_b16 v[220:221], v76
	ds_read_b128 v[20:23], v62 offset:48384
	ds_read_b128 v[224:227], v62 offset:55296
	ds_read_b64_tr_b16 v[222:223], v73
	ds_read_b64_tr_b16 v[228:229], v71
	ds_read_b64_tr_b16 v[230:231], v72
	s_waitcnt lgkmcnt(8)
	v_mfma_f32_16x16x32_bf16 v[118:121], v[212:215], v[16:19], v[118:121]
	ds_read_b128 v[232:235], v62 offset:50688
	s_waitcnt vmcnt(8)
	v_cvt_pk_bf16_f32 v12, v12, v13
	v_cvt_pk_bf16_f32 v13, v14, v15
	s_waitcnt lgkmcnt(7)
	v_mfma_f32_16x16x32_bf16 v[126:129], v[216:219], v[16:19], v[126:129]
	s_waitcnt vmcnt(7)
	v_cvt_pk_bf16_f32 v8, v8, v9
	v_cvt_pk_bf16_f32 v9, v10, v11
	s_waitcnt lgkmcnt(3)
	v_mfma_f32_16x16x32_bf16 v[152:155], v[220:223], v[16:19], v[152:155]
	s_waitcnt lgkmcnt(1)
	v_mfma_f32_16x16x32_bf16 v[164:167], v[228:231], v[16:19], v[164:167]
	v_lshl_add_u64 v[16:17], s[8:9], 0, v[146:147]
	v_lshl_add_u64 v[16:17], v[16:17], 0, s[10:11]
	v_lshl_add_u64 v[16:17], v[16:17], 0, v[132:133]
	v_lshl_add_u64 v[16:17], v[16:17], 0, v[148:149]
	v_lshl_add_u64 v[16:17], v[16:17], 0, v[150:151]
	v_add_co_u32_e32 v18, vcc, s16, v16
	v_mfma_f32_16x16x32_bf16 v[168:171], v[212:215], v[20:23], v[168:171]
	s_nop 0
	v_addc_co_u32_e32 v19, vcc, 0, v17, vcc
	global_load_dwordx4 v[28:31], v[16:17], off
	global_load_dwordx4 v[24:27], v[18:19], off
	v_add_co_u32_e32 v18, vcc, s17, v16
	v_mfma_f32_16x16x32_bf16 v[172:175], v[216:219], v[20:23], v[172:175]
	s_nop 0
	v_addc_co_u32_e32 v19, vcc, 0, v17, vcc
	v_add_co_u32_e32 v16, vcc, s18, v16
	v_mfma_f32_16x16x32_bf16 v[176:179], v[220:223], v[20:23], v[176:179]
	s_nop 0
	v_addc_co_u32_e32 v17, vcc, 0, v17, vcc
	ds_read_b128 v[236:239], v62 offset:52992
	v_mfma_f32_16x16x32_bf16 v[114:117], v[228:231], v[20:23], v[114:117]
	global_load_dwordx4 v[20:23], v[18:19], off
	s_nop 0
	global_load_dwordx4 v[16:19], v[16:17], off
	ds_write_b64 v240, v[12:13]
	ds_write_b64 v241, v[8:9]
	s_waitcnt lgkmcnt(3)
	v_mfma_f32_16x16x32_bf16 v[32:35], v[228:231], v[232:235], v[32:35]
	v_mfma_f32_16x16x32_bf16 v[188:191], v[212:215], v[232:235], v[188:191]
	v_mfma_f32_16x16x32_bf16 v[192:195], v[216:219], v[232:235], v[192:195]
	v_mfma_f32_16x16x32_bf16 v[196:199], v[220:223], v[232:235], v[196:199]
	s_waitcnt lgkmcnt(2)
	v_mfma_f32_16x16x32_bf16 v[8:11], v[212:215], v[236:239], v[36:39]
	s_waitcnt vmcnt(9)
	v_cvt_pk_bf16_f32 v0, v0, v1
	v_cvt_pk_bf16_f32 v1, v2, v3
	v_cvt_pk_bf16_f32 v130, v4, v5
	v_mfma_f32_16x16x32_bf16 v[12:15], v[216:219], v[236:239], v[180:183]
	v_cvt_pk_bf16_f32 v131, v6, v7
	v_mfma_f32_16x16x32_bf16 v[36:39], v[220:223], v[236:239], v[204:207]
	v_mfma_f32_16x16x32_bf16 v[180:183], v[228:231], v[236:239], v[184:187]
	s_nop 2
	ds_read_b128 v[184:187], v62 offset:46144
	ds_read_b128 v[204:207], v62 offset:48448
	v_mfma_f32_16x16x32_bf16 v[102:105], v[212:215], v[224:227], v[102:105]
	ds_read_b128 v[212:215], v62 offset:50752
	ds_write_b64 v243, v[0:1]
	ds_write_b64 v242, v[130:131]
	v_mfma_f32_16x16x32_bf16 v[106:109], v[216:219], v[224:227], v[106:109]
	v_mfma_f32_16x16x32_bf16 v[4:7], v[220:223], v[224:227], v[110:113]
	v_mfma_f32_16x16x32_bf16 v[0:3], v[228:231], v[224:227], v[122:125]
	s_nop 1
	ds_read_b64_tr_b16 v[110:111], v68
	ds_read_b64_tr_b16 v[112:113], v70
	ds_read_b64_tr_b16 v[122:123], v67
	ds_read_b64_tr_b16 v[124:125], v69
	ds_read_b64_tr_b16 v[216:217], v65
	ds_read_b64_tr_b16 v[218:219], v66
	ds_read_b64_tr_b16 v[220:221], v63
	ds_read_b64_tr_b16 v[222:223], v64
	s_waitcnt lgkmcnt(6)
	v_mfma_f32_16x16x32_bf16 v[118:121], v[110:113], v[184:187], v[118:121]
	s_waitcnt lgkmcnt(4)
	v_mfma_f32_16x16x32_bf16 v[126:129], v[122:125], v[184:187], v[126:129]
	s_waitcnt lgkmcnt(2)
	v_mfma_f32_16x16x32_bf16 v[152:155], v[216:219], v[184:187], v[152:155]
	s_waitcnt lgkmcnt(0)
	v_mfma_f32_16x16x32_bf16 v[164:167], v[220:223], v[184:187], v[164:167]
	v_mfma_f32_16x16x32_bf16 v[168:171], v[110:113], v[204:207], v[168:171]
	v_mfma_f32_16x16x32_bf16 v[172:175], v[122:125], v[204:207], v[172:175]
	v_mfma_f32_16x16x32_bf16 v[176:179], v[216:219], v[204:207], v[176:179]
	v_mfma_f32_16x16x32_bf16 v[114:117], v[220:223], v[204:207], v[114:117]
	v_mfma_f32_16x16x32_bf16 v[184:187], v[110:113], v[212:215], v[188:191]
	v_mfma_f32_16x16x32_bf16 v[188:191], v[122:125], v[212:215], v[192:195]
	v_mfma_f32_16x16x32_bf16 v[192:195], v[216:219], v[212:215], v[196:199]
	s_nop 2
	ds_read_b128 v[196:199], v62 offset:53056
	ds_read_b128 v[204:207], v62 offset:55360
	s_waitcnt vmcnt(8)
	ds_write_b128 v86, v[40:43]
	s_waitcnt vmcnt(7)
	ds_write_b128 v86, v[44:47] offset:9216
	v_mfma_f32_16x16x32_bf16 v[32:35], v[220:223], v[212:215], v[32:35]
	s_waitcnt lgkmcnt(3)
	v_mfma_f32_16x16x32_bf16 v[40:43], v[110:113], v[196:199], v[8:11]
	v_mfma_f32_16x16x32_bf16 v[44:47], v[122:125], v[196:199], v[12:15]
	v_mfma_f32_16x16x32_bf16 v[36:39], v[216:219], v[196:199], v[36:39]
	v_mfma_f32_16x16x32_bf16 v[180:183], v[220:223], v[196:199], v[180:183]
	s_waitcnt lgkmcnt(2)
	v_mfma_f32_16x16x32_bf16 v[102:105], v[110:113], v[204:207], v[102:105]
	v_mfma_f32_16x16x32_bf16 v[106:109], v[122:125], v[204:207], v[106:109]
	global_load_dwordx4 v[110:113], v[52:53], off offset:384
	s_nop 0
	global_load_dwordx4 v[52:55], v[54:55], off offset:384
	s_nop 0
	global_load_dwordx4 v[122:125], v[56:57], off offset:384
	s_nop 0
	global_load_dwordx4 v[56:59], v[58:59], off offset:384
	s_nop 0
	global_load_dwordx4 v[196:199], v[60:61], off offset:384
	s_waitcnt vmcnt(11)
	ds_write_b128 v86, v[48:51] offset:18432
	s_waitcnt vmcnt(10)
	ds_write_b128 v86, v[200:203] offset:27648
	s_waitcnt vmcnt(9)
	ds_write_b128 v86, v[208:211] offset:36864
	v_mfma_f32_16x16x32_bf16 v[48:51], v[220:223], v[204:207], v[0:3]
	v_mfma_f32_16x16x32_bf16 v[212:215], v[216:219], v[204:207], v[4:7]
	s_waitcnt lgkmcnt(0)
	s_barrier
	ds_read_b64_tr_b16 v[200:201], v81
	ds_read_b64_tr_b16 v[202:203], v82
	ds_read_b64_tr_b16 v[204:205], v83
	ds_read_b64_tr_b16 v[206:207], v84
	ds_read_b128 v[0:3], v62
	ds_read_b64_tr_b16 v[208:209], v79
	ds_read_b64_tr_b16 v[210:211], v80
	ds_read_b128 v[4:7], v62 offset:2304
	s_cmpk_lt_i32 s24, 0x100
	s_cselect_b32 s8, s24, 0
	s_waitcnt lgkmcnt(3)
	v_mfma_f32_16x16x32_bf16 v[80:83], v[200:203], v[0:3], v[118:121]
	s_nop 2
	ds_read_b64_tr_b16 v[118:119], v100
	ds_read_b64_tr_b16 v[120:121], v101
	s_cselect_b32 s10, s51, s57
	s_cselect_b32 s11, s50, s56
	s_ashr_i32 s9, s8, 31
	s_lshl_b64 s[8:9], s[8:9], 20
	s_add_u32 s8, s11, s8
	s_addc_u32 s9, s10, s9
	s_lshl_b32 s10, s25, 7
	s_ashr_i32 s11, s10, 31
	v_mfma_f32_16x16x32_bf16 v[126:129], v[204:207], v[0:3], v[126:129]
	s_lshl_b64 s[10:11], s[10:11], 2
	ds_read_b128 v[216:219], v62 offset:4608
	s_waitcnt vmcnt(8)
	v_cvt_pk_bf16_f32 v28, v28, v29
	s_waitcnt lgkmcnt(4)
	v_mfma_f32_16x16x32_bf16 v[152:155], v[208:211], v[0:3], v[152:155]
	v_cvt_pk_bf16_f32 v29, v30, v31
	s_waitcnt vmcnt(7)
	v_cvt_pk_bf16_f32 v24, v24, v25
	v_cvt_pk_bf16_f32 v25, v26, v27
	s_waitcnt lgkmcnt(1)
	v_mfma_f32_16x16x32_bf16 v[164:167], v[118:121], v[0:3], v[164:167]
	v_lshl_add_u64 v[0:1], s[8:9], 0, v[136:137]
	v_lshl_add_u64 v[0:1], v[0:1], 0, s[10:11]
	v_lshl_add_u64 v[0:1], v[0:1], 0, v[132:133]
	v_lshl_add_u64 v[0:1], v[0:1], 0, v[148:149]
	v_lshl_add_u64 v[8:9], v[0:1], 0, v[150:151]
	v_add_co_u32_e32 v0, vcc, s16, v8
	v_mfma_f32_16x16x32_bf16 v[168:171], v[200:203], v[4:7], v[168:171]
	s_nop 0
	v_addc_co_u32_e32 v1, vcc, 0, v9, vcc
	v_add_co_u32_e32 v10, vcc, s17, v8
	v_mfma_f32_16x16x32_bf16 v[172:175], v[204:207], v[4:7], v[172:175]
	s_nop 0
	v_addc_co_u32_e32 v11, vcc, 0, v9, vcc
	v_mfma_f32_16x16x32_bf16 v[176:179], v[208:211], v[4:7], v[176:179]
	v_mfma_f32_16x16x32_bf16 v[114:117], v[118:121], v[4:7], v[114:117]
	global_load_dwordx4 v[4:7], v[8:9], off
	s_nop 0
	global_load_dwordx4 v[0:3], v[0:1], off
	v_add_co_u32_e32 v8, vcc, s18, v8
	ds_read_b128 v[220:223], v62 offset:6912
	s_nop 0
	v_addc_co_u32_e32 v9, vcc, 0, v9, vcc
	global_load_dwordx4 v[12:15], v[10:11], off
	s_nop 0
	global_load_dwordx4 v[8:11], v[8:9], off
	ds_read_b128 v[224:227], v62 offset:9216
	s_waitcnt lgkmcnt(2)
	v_mfma_f32_16x16x32_bf16 v[32:35], v[118:121], v[216:219], v[32:35]
	ds_write_b64 v99, v[28:29]
	ds_write_b64 v98, v[24:25]
	v_mfma_f32_16x16x32_bf16 v[184:187], v[200:203], v[216:219], v[184:187]
	v_mfma_f32_16x16x32_bf16 v[188:191], v[204:207], v[216:219], v[188:191]
	v_mfma_f32_16x16x32_bf16 v[192:195], v[208:211], v[216:219], v[192:195]
	s_waitcnt lgkmcnt(3)
	v_mfma_f32_16x16x32_bf16 v[28:31], v[204:207], v[220:223], v[44:47]
	s_waitcnt vmcnt(9)
	v_cvt_pk_bf16_f32 v16, v16, v17
	v_cvt_pk_bf16_f32 v17, v18, v19
	v_cvt_pk_bf16_f32 v60, v20, v21
	s_waitcnt lgkmcnt(2)
	v_mfma_f32_16x16x32_bf16 v[44:47], v[200:203], v[224:227], v[102:105]
	ds_read_b128 v[98:101], v62 offset:64
	s_nop 1
	ds_read_b128 v[102:105], v62 offset:2368
	v_cvt_pk_bf16_f32 v61, v22, v23
	v_mfma_f32_16x16x32_bf16 v[24:27], v[200:203], v[220:223], v[40:43]
	v_mfma_f32_16x16x32_bf16 v[36:39], v[208:211], v[220:223], v[36:39]
	v_mfma_f32_16x16x32_bf16 v[40:43], v[118:121], v[220:223], v[180:183]
	v_mfma_f32_16x16x32_bf16 v[106:109], v[204:207], v[224:227], v[106:109]
	s_nop 1
	ds_read_b128 v[180:183], v62 offset:4672
	ds_write_b64 v92, v[16:17]
	ds_write_b64 v95, v[60:61]
	v_mfma_f32_16x16x32_bf16 v[20:23], v[208:211], v[224:227], v[212:215]
	v_mfma_f32_16x16x32_bf16 v[16:19], v[118:121], v[224:227], v[48:51]
	s_nop 2
	ds_read_b64_tr_b16 v[48:49], v91
	ds_read_b64_tr_b16 v[50:51], v93
	ds_read_b64_tr_b16 v[118:119], v89
	ds_read_b64_tr_b16 v[120:121], v90
	ds_read_b64_tr_b16 v[90:91], v85
	ds_read_b64_tr_b16 v[92:93], v94
	ds_read_b64_tr_b16 v[94:95], v96
	ds_read_b64_tr_b16 v[96:97], v97
	s_waitcnt lgkmcnt(6)
	v_mfma_f32_16x16x32_bf16 v[80:83], v[48:51], v[98:101], v[80:83]
	s_waitcnt lgkmcnt(4)
	v_mfma_f32_16x16x32_bf16 v[126:129], v[118:121], v[98:101], v[126:129]
	s_waitcnt lgkmcnt(2)
	v_mfma_f32_16x16x32_bf16 v[152:155], v[90:93], v[98:101], v[152:155]
	s_waitcnt lgkmcnt(0)
	v_mfma_f32_16x16x32_bf16 v[98:101], v[94:97], v[98:101], v[164:167]
	v_mfma_f32_16x16x32_bf16 v[164:167], v[48:51], v[102:105], v[168:171]
	v_mfma_f32_16x16x32_bf16 v[168:171], v[118:121], v[102:105], v[172:175]
	v_mfma_f32_16x16x32_bf16 v[172:175], v[90:93], v[102:105], v[176:179]
	v_mfma_f32_16x16x32_bf16 v[102:105], v[94:97], v[102:105], v[114:117]
	v_mfma_f32_16x16x32_bf16 v[114:117], v[48:51], v[180:183], v[184:187]
	v_mfma_f32_16x16x32_bf16 v[176:179], v[118:121], v[180:183], v[188:191]
	v_mfma_f32_16x16x32_bf16 v[184:187], v[90:93], v[180:183], v[192:195]
	s_nop 1
	ds_read_b128 v[188:191], v62 offset:6976
	ds_read_b128 v[192:195], v62 offset:9280
	s_waitcnt vmcnt(8)
	ds_write_b128 v86, v[110:113] offset:46080
	s_waitcnt vmcnt(7)
	ds_write_b128 v86, v[52:55] offset:55296
	v_mfma_f32_16x16x32_bf16 v[52:55], v[94:97], v[180:183], v[32:35]
	s_waitcnt lgkmcnt(3)
	v_mfma_f32_16x16x32_bf16 v[110:113], v[48:51], v[188:191], v[24:27]
	s_waitcnt vmcnt(6)
	ds_write_b128 v86, v[122:125] offset:64512
	s_waitcnt vmcnt(5)
	ds_write_b128 v87, v[56:59]
	s_waitcnt vmcnt(4)
	ds_write_b128 v88, v[196:199]
	v_mfma_f32_16x16x32_bf16 v[180:183], v[118:121], v[188:191], v[28:31]
	v_mfma_f32_16x16x32_bf16 v[200:203], v[90:93], v[188:191], v[36:39]
	v_mfma_f32_16x16x32_bf16 v[188:191], v[94:97], v[188:191], v[40:43]
	s_waitcnt lgkmcnt(5)
	v_mfma_f32_16x16x32_bf16 v[94:97], v[94:97], v[192:195], v[16:19]
	s_nop 2
	v_sub_u32_e32 v16, v163, v143
	v_xad_u32 v18, s26, -1, v16
	v_add_u32_e32 v17, s26, v162
	v_min_i32_e32 v16, 0, v18
	v_add_u32_e32 v19, v17, v143
	v_add_u32_e32 v16, v16, v19
	v_ashrrev_i32_e32 v17, 31, v16
	v_lshlrev_b64 v[16:17], 9, v[16:17]
	v_lshl_add_u64 v[16:17], v[134:135], 0, v[16:17]
	global_load_dwordx4 v[32:35], v[16:17], off
	v_min_i32_e32 v16, 64, v18
	v_add_u32_e32 v16, v16, v19
	v_ashrrev_i32_e32 v17, 31, v16
	v_lshlrev_b64 v[16:17], 9, v[16:17]
	v_lshl_add_u64 v[16:17], v[134:135], 0, v[16:17]
	global_load_dwordx4 v[36:39], v[16:17], off
	v_min_i32_e32 v16, 0x80, v18
	v_add_u32_e32 v16, v16, v19
	v_ashrrev_i32_e32 v17, 31, v16
	v_lshlrev_b64 v[16:17], 9, v[16:17]
	v_lshl_add_u64 v[16:17], v[134:135], 0, v[16:17]
	global_load_dwordx4 v[40:43], v[16:17], off
	v_min_i32_e32 v16, 0xc0, v18
	v_add_u32_e32 v16, v16, v19
	v_ashrrev_i32_e32 v17, 31, v16
	v_lshlrev_b64 v[16:17], 9, v[16:17]
	v_lshl_add_u64 v[16:17], v[134:135], 0, v[16:17]
	v_mfma_f32_16x16x32_bf16 v[204:207], v[48:51], v[192:195], v[44:47]
	s_nop 2
	global_load_dwordx4 v[44:47], v[16:17], off
	v_min_i32_e32 v16, 0x100, v18
	v_add_u32_e32 v16, v16, v19
	v_ashrrev_i32_e32 v17, 31, v16
	v_lshlrev_b64 v[16:17], 9, v[16:17]
	v_lshl_add_u64 v[16:17], v[134:135], 0, v[16:17]
	global_load_dwordx4 v[48:51], v[16:17], off
	v_mfma_f32_16x16x32_bf16 v[106:109], v[118:121], v[192:195], v[106:109]
	v_mfma_f32_16x16x32_bf16 v[90:93], v[90:93], v[192:195], v[20:23]
	s_waitcnt lgkmcnt(0)
	s_barrier
	ds_read_b64_tr_b16 v[56:57], v77
	ds_read_b64_tr_b16 v[58:59], v78
	ds_read_b128 v[16:19], v62 offset:46080
	ds_read_b64_tr_b16 v[84:85], v74
	ds_read_b64_tr_b16 v[86:87], v75
	ds_read_b64_tr_b16 v[74:75], v76
	ds_read_b128 v[20:23], v62 offset:48384
	ds_read_b128 v[118:121], v62 offset:55296
	ds_read_b64_tr_b16 v[76:77], v73
	s_waitcnt lgkmcnt(4)
	v_mfma_f32_16x16x32_bf16 v[122:125], v[84:87], v[16:19], v[126:129]
	s_nop 2
	ds_read_b64_tr_b16 v[126:127], v71
	ds_read_b64_tr_b16 v[128:129], v72
	ds_read_b128 v[192:195], v62 offset:50688
	v_mfma_f32_16x16x32_bf16 v[78:81], v[56:59], v[16:19], v[80:83]
	s_waitcnt lgkmcnt(3)
	v_mfma_f32_16x16x32_bf16 v[152:155], v[74:77], v[16:19], v[152:155]
	s_waitcnt lgkmcnt(1)
	v_mfma_f32_16x16x32_bf16 v[98:101], v[126:129], v[16:19], v[98:101]
	v_lshl_add_u64 v[16:17], s[8:9], 0, v[138:139]
	v_lshl_add_u64 v[16:17], v[16:17], 0, s[10:11]
	v_lshl_add_u64 v[16:17], v[16:17], 0, v[132:133]
	v_lshl_add_u64 v[16:17], v[16:17], 0, v[148:149]
	v_lshl_add_u64 v[16:17], v[16:17], 0, v[150:151]
	v_add_co_u32_e32 v18, vcc, s16, v16
	v_mfma_f32_16x16x32_bf16 v[164:167], v[56:59], v[20:23], v[164:167]
	s_nop 0
	v_addc_co_u32_e32 v19, vcc, 0, v17, vcc
	global_load_dwordx4 v[28:31], v[16:17], off
	global_load_dwordx4 v[24:27], v[18:19], off
	v_add_co_u32_e32 v18, vcc, s17, v16
	v_mfma_f32_16x16x32_bf16 v[168:171], v[84:87], v[20:23], v[168:171]
	s_nop 0
	v_addc_co_u32_e32 v19, vcc, 0, v17, vcc
	v_add_co_u32_e32 v16, vcc, s18, v16
	v_mfma_f32_16x16x32_bf16 v[172:175], v[74:77], v[20:23], v[172:175]
	s_nop 0
	v_addc_co_u32_e32 v17, vcc, 0, v17, vcc
	v_mfma_f32_16x16x32_bf16 v[196:199], v[126:129], v[20:23], v[102:105]
	s_nop 2
	ds_read_b128 v[102:105], v62 offset:52992
	global_load_dwordx4 v[20:23], v[18:19], off
	s_nop 0
	global_load_dwordx4 v[16:19], v[16:17], off
	s_waitcnt lgkmcnt(1)
	v_mfma_f32_16x16x32_bf16 v[52:55], v[126:129], v[192:195], v[52:55]
	v_mfma_f32_16x16x32_bf16 v[208:211], v[56:59], v[192:195], v[114:117]
	v_mfma_f32_16x16x32_bf16 v[176:179], v[84:87], v[192:195], v[176:179]
	v_mfma_f32_16x16x32_bf16 v[184:187], v[74:77], v[192:195], v[184:187]
	s_waitcnt lgkmcnt(0)
	v_mfma_f32_16x16x32_bf16 v[192:195], v[56:59], v[102:105], v[110:113]
	v_mfma_f32_16x16x32_bf16 v[180:183], v[84:87], v[102:105], v[180:183]
	v_mfma_f32_16x16x32_bf16 v[200:203], v[74:77], v[102:105], v[200:203]
	v_mfma_f32_16x16x32_bf16 v[56:59], v[56:59], v[118:121], v[204:207]
	v_mfma_f32_16x16x32_bf16 v[204:207], v[84:87], v[118:121], v[106:109]
	v_mfma_f32_16x16x32_bf16 v[212:215], v[74:77], v[118:121], v[90:93]
	ds_read_b128 v[72:75], v62 offset:46144
	ds_read_b128 v[82:85], v62 offset:48448
	s_nop 0
	ds_read_b128 v[88:91], v62 offset:50752
	v_mfma_f32_16x16x32_bf16 v[188:191], v[126:129], v[102:105], v[188:191]
	v_mfma_f32_16x16x32_bf16 v[216:219], v[126:129], v[118:121], v[94:97]
	ds_read_b64_tr_b16 v[220:221], v68
	ds_read_b64_tr_b16 v[222:223], v70
	ds_read_b64_tr_b16 v[224:225], v67
	ds_read_b64_tr_b16 v[226:227], v69
	ds_read_b64_tr_b16 v[228:229], v65
	ds_read_b64_tr_b16 v[230:231], v66
	ds_read_b64_tr_b16 v[232:233], v63
	ds_read_b64_tr_b16 v[234:235], v64
	s_waitcnt lgkmcnt(6)
	v_mfma_f32_16x16x32_bf16 v[116:119], v[220:223], v[72:75], v[78:81]
	s_waitcnt lgkmcnt(4)
	v_mfma_f32_16x16x32_bf16 v[128:131], v[224:227], v[72:75], v[122:125]
	s_waitcnt lgkmcnt(2)
	v_mfma_f32_16x16x32_bf16 v[120:123], v[228:231], v[72:75], v[152:155]
	ds_read_b128 v[64:67], v62 offset:53056
	s_nop 1
	ds_read_b128 v[152:155], v62 offset:55360
	s_waitcnt lgkmcnt(2)
	v_mfma_f32_16x16x32_bf16 v[124:127], v[232:235], v[72:75], v[98:101]
	v_mfma_f32_16x16x32_bf16 v[112:115], v[220:223], v[82:85], v[164:167]
	v_mfma_f32_16x16x32_bf16 v[108:111], v[224:227], v[82:85], v[168:171]
	v_mfma_f32_16x16x32_bf16 v[104:107], v[228:231], v[82:85], v[172:175]
	v_mfma_f32_16x16x32_bf16 v[100:103], v[232:235], v[82:85], v[196:199]
	v_mfma_f32_16x16x32_bf16 v[96:99], v[220:223], v[88:91], v[208:211]
	v_mfma_f32_16x16x32_bf16 v[92:95], v[224:227], v[88:91], v[176:179]
	v_mfma_f32_16x16x32_bf16 v[84:87], v[228:231], v[88:91], v[184:187]
	v_mfma_f32_16x16x32_bf16 v[88:91], v[232:235], v[88:91], v[52:55]
	s_waitcnt lgkmcnt(1)
	v_mfma_f32_16x16x32_bf16 v[80:83], v[220:223], v[64:67], v[192:195]
	v_mfma_f32_16x16x32_bf16 v[76:79], v[224:227], v[64:67], v[180:183]
	v_mfma_f32_16x16x32_bf16 v[72:75], v[228:231], v[64:67], v[200:203]
	v_mfma_f32_16x16x32_bf16 v[68:71], v[232:235], v[64:67], v[188:191]
	s_waitcnt lgkmcnt(0)
	v_mfma_f32_16x16x32_bf16 v[64:67], v[220:223], v[152:155], v[56:59]
	v_mfma_f32_16x16x32_bf16 v[60:63], v[224:227], v[152:155], v[204:207]
	v_mfma_f32_16x16x32_bf16 v[56:59], v[228:231], v[152:155], v[212:215]
	v_mfma_f32_16x16x32_bf16 v[52:55], v[232:235], v[152:155], v[216:219]
	v_add_u32_e32 v149, s14, v157
	v_cmp_lt_i32_e32 vcc, v149, v156
	v_lshlrev_b32_e32 v154, 1, v140
	v_lshlrev_b32_e32 v152, 1, v142
	s_and_saveexec_b64 s[8:9], vcc
	s_cbranch_execz .LBB0_908
	v_add_u32_e32 v164, v141, v149
	v_ashrrev_i32_e32 v165, 31, v164
	v_readlane_b32 s10, v254, 3
	v_lshlrev_b64 v[164:165], 11, v[164:165]
	v_readlane_b32 s11, v254, 4
	v_mov_b32_e32 v155, v133
	v_mov_b32_e32 v153, v133
	v_lshl_add_u64 v[164:165], s[10:11], 0, v[164:165]
	v_lshl_add_u64 v[164:165], s[6:7], 1, v[164:165]
	v_lshl_add_u64 v[164:165], v[164:165], 0, v[154:155]
	v_lshl_add_u64 v[164:165], v[164:165], 0, v[152:153]
	v_cvt_pk_bf16_f32 v116, v116, v117
	v_cvt_pk_bf16_f32 v117, v118, v119
	v_cvt_pk_bf16_f32 v118, v128, v129
	v_cvt_pk_bf16_f32 v119, v130, v131
	global_store_dwordx4 v[164:165], v[116:119], off nt
	s_nop 1
	v_cvt_pk_bf16_f32 v116, v120, v121
	v_cvt_pk_bf16_f32 v117, v122, v123
	v_cvt_pk_bf16_f32 v118, v124, v125
	v_cvt_pk_bf16_f32 v119, v126, v127
	global_store_dwordx4 v[164:165], v[116:119], off offset:16 nt
.LBB0_908:
	s_or_b64 exec, exec, s[8:9]
	s_nop 0
	v_add_u32_e32 v116, s14, v158
	v_cmp_lt_i32_e32 vcc, v116, v156
	s_and_saveexec_b64 s[8:9], vcc
	s_cbranch_execz .LBB0_910
	v_add_u32_e32 v116, v141, v116
	v_ashrrev_i32_e32 v117, 31, v116
	v_readlane_b32 s10, v254, 3
	v_lshlrev_b64 v[116:117], 11, v[116:117]
	v_readlane_b32 s11, v254, 4
	v_mov_b32_e32 v155, v133
	v_mov_b32_e32 v153, v133
	v_lshl_add_u64 v[116:117], s[10:11], 0, v[116:117]
	v_lshl_add_u64 v[116:117], s[6:7], 1, v[116:117]
	v_lshl_add_u64 v[116:117], v[116:117], 0, v[154:155]
	v_lshl_add_u64 v[116:117], v[116:117], 0, v[152:153]
	v_cvt_pk_bf16_f32 v112, v112, v113
	v_cvt_pk_bf16_f32 v113, v114, v115
	v_cvt_pk_bf16_f32 v114, v108, v109
	v_cvt_pk_bf16_f32 v115, v110, v111
	v_cvt_pk_bf16_f32 v104, v104, v105
	v_cvt_pk_bf16_f32 v105, v106, v107
	v_cvt_pk_bf16_f32 v106, v100, v101
	v_cvt_pk_bf16_f32 v107, v102, v103
	global_store_dwordx4 v[116:117], v[112:115], off nt
	global_store_dwordx4 v[116:117], v[104:107], off offset:16 nt
.LBB0_910:
	s_or_b64 exec, exec, s[8:9]
	v_add_u32_e32 v100, s14, v159
	v_cmp_lt_i32_e32 vcc, v100, v156
	s_and_saveexec_b64 s[8:9], vcc
	s_cbranch_execz .LBB0_912
	v_add_u32_e32 v100, v141, v100
	v_ashrrev_i32_e32 v101, 31, v100
	v_readlane_b32 s10, v254, 3
	v_lshlrev_b64 v[100:101], 11, v[100:101]
	v_readlane_b32 s11, v254, 4
	v_mov_b32_e32 v155, v133
	v_mov_b32_e32 v153, v133
	v_lshl_add_u64 v[100:101], s[10:11], 0, v[100:101]
	v_lshl_add_u64 v[100:101], s[6:7], 1, v[100:101]
	v_lshl_add_u64 v[100:101], v[100:101], 0, v[154:155]
	v_lshl_add_u64 v[100:101], v[100:101], 0, v[152:153]
	v_cvt_pk_bf16_f32 v96, v96, v97
	v_cvt_pk_bf16_f32 v97, v98, v99
	v_cvt_pk_bf16_f32 v98, v92, v93
	v_cvt_pk_bf16_f32 v99, v94, v95
	v_cvt_pk_bf16_f32 v84, v84, v85
	v_cvt_pk_bf16_f32 v85, v86, v87
	v_cvt_pk_bf16_f32 v86, v88, v89
	v_cvt_pk_bf16_f32 v87, v90, v91
	global_store_dwordx4 v[100:101], v[96:99], off nt
	global_store_dwordx4 v[100:101], v[84:87], off offset:16 nt
.LBB0_912:
	s_or_b64 exec, exec, s[8:9]
	s_nop 0
	v_add_u32_e32 v84, s14, v160
	v_cmp_lt_i32_e32 vcc, v84, v156
	s_and_saveexec_b64 s[8:9], vcc
	s_cbranch_execz .LBB0_914
	v_add_u32_e32 v84, v141, v84
	v_ashrrev_i32_e32 v85, 31, v84
	v_readlane_b32 s10, v254, 3
	v_lshlrev_b64 v[84:85], 11, v[84:85]
	v_readlane_b32 s11, v254, 4
	v_mov_b32_e32 v155, v133
	v_mov_b32_e32 v153, v133
	v_lshl_add_u64 v[84:85], s[10:11], 0, v[84:85]
	v_lshl_add_u64 v[84:85], s[6:7], 1, v[84:85]
	v_lshl_add_u64 v[84:85], v[84:85], 0, v[154:155]
	v_lshl_add_u64 v[84:85], v[84:85], 0, v[152:153]
	v_cvt_pk_bf16_f32 v80, v80, v81
	v_cvt_pk_bf16_f32 v81, v82, v83
	v_cvt_pk_bf16_f32 v82, v76, v77
	v_cvt_pk_bf16_f32 v83, v78, v79
	v_cvt_pk_bf16_f32 v72, v72, v73
	v_cvt_pk_bf16_f32 v73, v74, v75
	v_cvt_pk_bf16_f32 v74, v68, v69
	v_cvt_pk_bf16_f32 v75, v70, v71
	global_store_dwordx4 v[84:85], v[80:83], off nt
	global_store_dwordx4 v[84:85], v[72:75], off offset:16 nt

.LBB0_916:
	v_add_u32_e32 v68, v141, v68
	v_ashrrev_i32_e32 v69, 31, v68
	v_readlane_b32 s10, v254, 3
	v_lshlrev_b64 v[68:69], 11, v[68:69]
	v_readlane_b32 s11, v254, 4
	v_mov_b32_e32 v155, v133
	v_mov_b32_e32 v153, v133
	v_lshl_add_u64 v[68:69], s[10:11], 0, v[68:69]
	v_lshl_add_u64 v[68:69], s[6:7], 1, v[68:69]
	v_lshl_add_u64 v[68:69], v[68:69], 0, v[154:155]
	v_lshl_add_u64 v[68:69], v[68:69], 0, v[152:153]
	v_cvt_pk_bf16_f32 v64, v64, v65
	v_cvt_pk_bf16_f32 v65, v66, v67
	v_cvt_pk_bf16_f32 v66, v60, v61
	v_cvt_pk_bf16_f32 v67, v62, v63
	v_cvt_pk_bf16_f32 v56, v56, v57
	v_cvt_pk_bf16_f32 v57, v58, v59
	v_cvt_pk_bf16_f32 v58, v52, v53
	v_cvt_pk_bf16_f32 v59, v54, v55
	global_store_dwordx4 v[68:69], v[64:67], off nt
	global_store_dwordx4 v[68:69], v[56:59], off offset:16 nt
	s_or_b64 exec, exec, s[8:9]
	s_andn2_b64 vcc, exec, s[4:5]
	s_cbranch_vccnz .LBB0_901

.LBB0_2485:
	s_waitcnt lgkmcnt(0)
	v_mov_b32_e32 v52, v244
	v_mov_b32_e32 v53, 0
	s_waitcnt vmcnt(7)
	v_cvt_pk_bf16_f32 v20, v20, v21
	v_mbcnt_lo_u32_b32 v53, -1, v53
	v_mbcnt_hi_u32_b32 v53, -1, v53
	s_waitcnt lgkmcnt(0)
	v_readfirstlane_b32 s6, v52
	v_cvt_pk_bf16_f32 v21, v22, v23
	s_waitcnt vmcnt(6)
	v_cvt_pk_bf16_f32 v16, v16, v17
	v_lshl_or_b32 v62, s6, 6, v53
	v_cvt_pk_bf16_f32 v17, v18, v19
	v_lshrrev_b32_e32 v53, 3, v62
	v_lshlrev_b32_e32 v54, 4, v62
	v_and_b32_e32 v68, 0x70, v54
	v_mul_lo_u32 v69, v53, s22
	v_ashrrev_i32_e32 v52, 5, v62
	v_add3_u32 v53, 0, v68, v69
	ds_write_b128 v53, v[36:39]
	ds_write_b128 v53, v[32:35] offset:9216
	ds_write_b128 v53, v[44:47] offset:18432
	s_waitcnt vmcnt(5)
	ds_write_b128 v53, v[40:43] offset:27648
	s_waitcnt vmcnt(4)
	ds_write_b128 v53, v[48:51] offset:36864
	v_lshrrev_b32_e32 v34, 1, v52
	v_bfe_u32 v32, v62, 2, 3
	v_and_b32_e32 v33, 3, v52
	v_and_b32_e32 v34, 4, v34
	v_bitop3_b32 v32, v34, v32, v33 bitop3:0x36
	v_lshlrev_b32_e32 v33, 2, v62
	v_and_b32_e32 v36, 12, v33
	v_lshlrev_b32_e32 v37, 1, v36
	v_lshl_or_b32 v70, v32, 5, v37
	v_lshlrev_b32_e32 v172, 8, v52
	v_add3_u32 v22, s23, v70, v172
	ds_write2st64_b64 v22, v[20:21], v[16:17] offset1:8
	s_waitcnt vmcnt(5)
	v_cvt_pk_bf16_f32 v16, v28, v29
	v_cvt_pk_bf16_f32 v17, v30, v31
	s_waitcnt vmcnt(4)
	v_cvt_pk_bf16_f32 v18, v24, v25
	v_cvt_pk_bf16_f32 v19, v26, v27
	ds_write2st64_b64 v22, v[16:17], v[18:19] offset0:16 offset1:24
	v_sub_u32_e32 v16, v156, v143
	v_xad_u32 v32, s14, -1, v16
	v_add_u32_e32 v17, s14, v141
	v_lshrrev_b32_e32 v39, 2, v62
	v_bfe_u32 v65, v62, 2, 2
	v_min_i32_e32 v16, 0, v32
	v_add_u32_e32 v33, v17, v143
	v_and_b32_e32 v39, 4, v39
	v_bfe_u32 v66, v62, 6, 1
	v_add_u32_e32 v16, v16, v33
	v_or_b32_e32 v40, v39, v65
	v_ashrrev_i32_e32 v17, 31, v16
	v_lshlrev_b32_e32 v41, 6, v66
	v_lshlrev_b32_e32 v40, 4, v40
	v_lshlrev_b64 v[16:17], 9, v[16:17]
	v_lshrrev_b32_e32 v38, 1, v62
	v_xor_b32_e32 v40, v40, v41
	s_cmpk_lt_i32 s13, 0x100
	v_readlane_b32 s36, v253, 4
	v_lshl_add_u64 v[52:53], v[134:135], 0, v[16:17]
	v_min_i32_e32 v16, 64, v32
	v_and_b32_e32 v67, 24, v38
	v_or_b32_e32 v36, v40, v36
	s_cselect_b32 s6, s13, 1
	v_readlane_b32 s48, v253, 16
	v_readlane_b32 s49, v253, 17
	v_add_u32_e32 v16, v16, v33
	v_or_b32_e32 v38, v67, v65
	v_lshlrev_b32_e32 v188, 1, v36
	v_lshlrev_b32_e32 v36, 2, v66
	s_cselect_b32 s9, s17, s49
	s_cselect_b32 s8, s16, s48
	s_ashr_i32 s7, s6, 31
	v_ashrrev_i32_e32 v17, 31, v16
	v_lshlrev_b32_e32 v71, 8, v38
	v_or_b32_e32 v38, 1, v36
	s_lshl_b64 s[6:7], s[6:7], 20
	v_lshlrev_b64 v[16:17], 9, v[16:17]
	v_bitop3_b32 v38, v39, v38, v65 bitop3:0x36
	s_add_u32 s8, s8, s6
	v_lshl_add_u64 v[54:55], v[134:135], 0, v[16:17]
	v_min_i32_e32 v16, 0x80, v32
	v_lshl_or_b32 v192, v38, 5, v37
	v_or_b32_e32 v38, 2, v36
	v_or_b32_e32 v36, 3, v36
	s_addc_u32 s9, s9, s7
	s_lshl_b32 s6, s15, 7
	v_add_u32_e32 v16, v16, v33
	v_bitop3_b32 v38, v39, v38, v65 bitop3:0x36
	v_bitop3_b32 v36, v39, v36, v65 bitop3:0x36
	s_ashr_i32 s7, s6, 31
	v_ashrrev_i32_e32 v17, 31, v16
	v_lshl_or_b32 v193, v38, 5, v37
	v_lshl_or_b32 v196, v36, 5, v37
	v_lshl_add_u64 v[36:37], s[8:9], 0, v[144:145]
	s_lshl_b64 s[10:11], s[6:7], 2
	v_lshlrev_b64 v[16:17], 9, v[16:17]
	v_lshl_add_u64 v[36:37], v[36:37], 0, s[10:11]
	v_lshl_add_u64 v[56:57], v[134:135], 0, v[16:17]
	v_min_i32_e32 v16, 0xc0, v32
	v_min_i32_e32 v32, 0x100, v32
	v_lshl_add_u64 v[36:37], v[36:37], 0, v[132:133]
	v_mov_b32_e32 v149, v133
	v_add_u32_e32 v32, v32, v33
	v_lshl_add_u64 v[36:37], v[36:37], 0, v[148:149]
	v_mov_b32_e32 v151, v133
	v_add_u32_e32 v16, v16, v33
	v_ashrrev_i32_e32 v33, 31, v32
	v_lshl_add_u64 v[36:37], v[36:37], 0, v[150:151]
	v_ashrrev_i32_e32 v17, 31, v16
	v_lshlrev_b64 v[32:33], 9, v[32:33]
	v_add_co_u32_e32 v38, vcc, s18, v36
	v_lshlrev_b64 v[16:17], 9, v[16:17]
	v_lshl_add_u64 v[60:61], v[134:135], 0, v[32:33]
	v_addc_co_u32_e32 v39, vcc, 0, v37, vcc
	global_load_dwordx4 v[24:27], v[52:53], off offset:128
	global_load_dwordx4 v[28:31], v[54:55], off offset:128
	v_lshl_add_u64 v[58:59], v[134:135], 0, v[16:17]
	global_load_dwordx4 v[16:19], v[56:57], off offset:128
	global_load_dwordx4 v[20:23], v[58:59], off offset:128
	global_load_dwordx4 v[32:35], v[60:61], off offset:128
	s_waitcnt lgkmcnt(0)
	s_barrier
	global_load_dwordx4 v[48:51], v[36:37], off
	global_load_dwordx4 v[44:47], v[38:39], off
	v_add_co_u32_e32 v38, vcc, s19, v36
	v_ashrrev_i32_e32 v63, 7, v62
	s_nop 0
	v_addc_co_u32_e32 v39, vcc, 0, v37, vcc
	v_add_co_u32_e32 v36, vcc, s20, v36
	v_and_b32_e32 v64, 15, v62
	s_nop 0
	v_addc_co_u32_e32 v37, vcc, 0, v37, vcc
	global_load_dwordx4 v[40:43], v[38:39], off
	s_nop 0
	global_load_dwordx4 v[36:39], v[36:37], off
	v_add_u32_e32 v62, s23, v71
	v_add_u32_e32 v84, v62, v188
	v_add_u32_e32 v86, v62, v192
	v_add_u32_e32 v82, v62, v193
	v_add_u32_e32 v236, v62, v196
	v_mul_lo_u32 v62, v63, s21
	v_add_u32_e32 v189, 0, v71
	v_or_b32_e32 v62, v62, v64
	v_add_u32_e32 v72, 0x16c00, v189
	v_lshlrev_b32_e32 v63, 1, v67
	v_mul_lo_u32 v62, v62, s22
	v_add_u32_e32 v85, v72, v188
	v_add_u32_e32 v87, v72, v192
	v_add_u32_e32 v83, v72, v193
	v_add_u32_e32 v237, v72, v196
	v_add3_u32 v62, 0, v63, v62
	ds_read_b64_tr_b16 v[100:101], v84
	ds_read_b64_tr_b16 v[102:103], v85
	ds_read_b64_tr_b16 v[104:105], v86
	ds_read_b64_tr_b16 v[106:107], v87
	ds_read_b128 v[64:67], v62
	ds_read_b64_tr_b16 v[108:109], v82
	ds_read_b64_tr_b16 v[110:111], v83
	ds_read_b128 v[112:115], v62 offset:2304
	ds_read_b64_tr_b16 v[120:121], v236
	ds_read_b64_tr_b16 v[122:123], v237
	v_add3_u32 v63, 0, v172, v70
	v_or_b32_e32 v197, 0x2000, v71
	v_add_u32_e32 v72, 0x18c00, v189
	s_waitcnt lgkmcnt(5)
	v_mfma_f32_16x16x32_bf16 v[116:119], v[100:103], v[64:67], 0
	v_add3_u32 v79, 0, v69, v68
	v_add_u32_e32 v68, s24, v71
	ds_read_b128 v[176:179], v62 offset:4608
	ds_read_b128 v[180:183], v62 offset:6912
	v_mfma_f32_16x16x32_bf16 v[124:127], v[104:107], v[64:67], 0
	v_add3_u32 v99, s24, v172, v70
	v_add_u32_e32 v98, 0x1b800, v63
	v_add_u32_e32 v95, 0x1c800, v63
	s_waitcnt lgkmcnt(5)
	v_mfma_f32_16x16x32_bf16 v[128:131], v[108:111], v[64:67], 0
	v_add_u32_e32 v92, 0x1d800, v63
	v_add3_u32 v91, s23, v188, v197
	v_add_u32_e32 v93, v72, v188
	s_waitcnt lgkmcnt(2)
	v_mfma_f32_16x16x32_bf16 v[152:155], v[120:123], v[64:67], 0
	v_add_u32_e32 v64, 0x1ac00, v189
	v_add_u32_e32 v66, 0x1cc00, v189
	v_add3_u32 v89, s23, v192, v197
	v_add_u32_e32 v90, v72, v192
	v_add3_u32 v88, s23, v193, v197
	v_add_u32_e32 v94, v72, v193
	v_add3_u32 v96, s23, v196, v197
	v_add_u32_e32 v97, v72, v196
	v_add_u32_e32 v77, v68, v188
	v_add_u32_e32 v78, v64, v188
	v_add_u32_e32 v74, v68, v192
	v_mfma_f32_16x16x32_bf16 v[164:167], v[100:103], v[112:115], 0
	v_add_u32_e32 v75, v64, v192
	v_add_u32_e32 v76, v68, v193
	v_add_u32_e32 v71, v64, v193
	v_mfma_f32_16x16x32_bf16 v[168:171], v[104:107], v[112:115], 0
	v_add_u32_e32 v72, v68, v196
	v_add_u32_e32 v73, v64, v196
	v_add3_u32 v238, s23, v172, v70
	v_mfma_f32_16x16x32_bf16 v[172:175], v[108:111], v[112:115], 0
	v_add_u32_e32 v239, 0x17800, v63
	v_add_u32_e32 v240, 0x18800, v63
	v_add_u32_e32 v241, 0x19800, v63
	v_mfma_f32_16x16x32_bf16 v[112:115], v[120:123], v[112:115], 0
	v_add3_u32 v68, s24, v188, v197
	v_add_u32_e32 v70, v66, v188
	v_add3_u32 v67, s24, v192, v197
	v_add_u32_e32 v69, v66, v192
	v_add3_u32 v63, s24, v193, v197
	v_add_u32_e32 v64, v66, v193
	v_add3_u32 v65, s24, v196, v197
	v_add_u32_e32 v66, v66, v196
	ds_read_b128 v[196:199], v62 offset:9216
	v_add_u32_e32 v80, 0x12000, v79
	v_add_u32_e32 v81, 0x14400, v79
	s_waitcnt vmcnt(12)
	v_cvt_pk_bf16_f32 v12, v12, v13
	v_cvt_pk_bf16_f32 v13, v14, v15
	s_waitcnt vmcnt(11)
	v_cvt_pk_bf16_f32 v8, v8, v9
	v_cvt_pk_bf16_f32 v9, v10, v11
	v_readlane_b32 s37, v253, 5
	v_readlane_b32 s38, v253, 6
	v_readlane_b32 s39, v253, 7
	v_readlane_b32 s40, v253, 8
	v_readlane_b32 s41, v253, 9
	v_readlane_b32 s42, v253, 10
	v_readlane_b32 s43, v253, 11
	v_readlane_b32 s44, v253, 12
	v_readlane_b32 s45, v253, 13
	v_readlane_b32 s46, v253, 14
	v_readlane_b32 s47, v253, 15
	v_readlane_b32 s50, v253, 18
	v_readlane_b32 s51, v253, 19
	s_waitcnt lgkmcnt(2)
	v_mfma_f32_16x16x32_bf16 v[184:187], v[100:103], v[176:179], 0
	ds_write_b64 v99, v[12:13]
	ds_write_b64 v98, v[8:9]
	v_mfma_f32_16x16x32_bf16 v[188:191], v[104:107], v[176:179], 0
	v_mfma_f32_16x16x32_bf16 v[192:195], v[108:111], v[176:179], 0
	v_mfma_f32_16x16x32_bf16 v[176:179], v[120:123], v[176:179], 0
	ds_read_b128 v[204:207], v62 offset:64
	ds_read_b128 v[208:211], v62 offset:2368
	s_waitcnt vmcnt(9)
	v_cvt_pk_bf16_f32 v0, v0, v1
	v_cvt_pk_bf16_f32 v1, v2, v3
	s_waitcnt lgkmcnt(5)
	v_mfma_f32_16x16x32_bf16 v[8:11], v[100:103], v[180:183], 0
	ds_read_b128 v[212:215], v62 offset:4672
	v_cvt_pk_bf16_f32 v216, v4, v5
	v_cvt_pk_bf16_f32 v217, v6, v7
	v_mfma_f32_16x16x32_bf16 v[12:15], v[104:107], v[180:183], 0
	ds_write_b64 v92, v[0:1]
	ds_write_b64 v95, v[216:217]
	s_waitcnt lgkmcnt(7)
	v_mfma_f32_16x16x32_bf16 v[100:103], v[100:103], v[196:199], 0
	v_mfma_f32_16x16x32_bf16 v[104:107], v[104:107], v[196:199], 0
	v_mfma_f32_16x16x32_bf16 v[4:7], v[108:111], v[196:199], 0
	v_mfma_f32_16x16x32_bf16 v[0:3], v[120:123], v[196:199], 0
	v_mfma_f32_16x16x32_bf16 v[200:203], v[108:111], v[180:183], 0
	v_mfma_f32_16x16x32_bf16 v[180:183], v[120:123], v[180:183], 0
	ds_read_b64_tr_b16 v[108:109], v91
	ds_read_b64_tr_b16 v[110:111], v93
	ds_read_b64_tr_b16 v[120:121], v89
	ds_read_b64_tr_b16 v[122:123], v90
	ds_read_b64_tr_b16 v[196:197], v88
	ds_read_b64_tr_b16 v[198:199], v94
	ds_read_b64_tr_b16 v[216:217], v96
	ds_read_b64_tr_b16 v[218:219], v97
	s_waitcnt lgkmcnt(6)
	v_mfma_f32_16x16x32_bf16 v[116:119], v[108:111], v[204:207], v[116:119]
	s_waitcnt lgkmcnt(4)
	v_mfma_f32_16x16x32_bf16 v[124:127], v[120:123], v[204:207], v[124:127]
	s_waitcnt lgkmcnt(2)
	v_mfma_f32_16x16x32_bf16 v[128:131], v[196:199], v[204:207], v[128:131]
	s_waitcnt lgkmcnt(0)
	v_mfma_f32_16x16x32_bf16 v[152:155], v[216:219], v[204:207], v[152:155]
	v_mfma_f32_16x16x32_bf16 v[164:167], v[108:111], v[208:211], v[164:167]
	v_mfma_f32_16x16x32_bf16 v[168:171], v[120:123], v[208:211], v[168:171]
	v_mfma_f32_16x16x32_bf16 v[172:175], v[196:199], v[208:211], v[172:175]
	v_mfma_f32_16x16x32_bf16 v[112:115], v[216:219], v[208:211], v[112:115]
	ds_read_b128 v[204:207], v62 offset:6976
	ds_read_b128 v[208:211], v62 offset:9280
	s_waitcnt vmcnt(8)
	ds_write_b128 v79, v[24:27] offset:46080
	s_waitcnt vmcnt(7)
	ds_write_b128 v79, v[28:31] offset:55296
	v_mfma_f32_16x16x32_bf16 v[24:27], v[216:219], v[212:215], v[176:179]
	v_mfma_f32_16x16x32_bf16 v[184:187], v[108:111], v[212:215], v[184:187]
	v_mfma_f32_16x16x32_bf16 v[188:191], v[120:123], v[212:215], v[188:191]
	v_mfma_f32_16x16x32_bf16 v[192:195], v[196:199], v[212:215], v[192:195]
	s_waitcnt lgkmcnt(3)
	v_mfma_f32_16x16x32_bf16 v[8:11], v[108:111], v[204:207], v[8:11]
	v_mfma_f32_16x16x32_bf16 v[28:31], v[120:123], v[204:207], v[12:15]
	v_mfma_f32_16x16x32_bf16 v[176:179], v[196:199], v[204:207], v[200:203]
	v_mfma_f32_16x16x32_bf16 v[180:183], v[216:219], v[204:207], v[180:183]
	s_waitcnt lgkmcnt(2)
	v_mfma_f32_16x16x32_bf16 v[100:103], v[108:111], v[208:211], v[100:103]
	v_mfma_f32_16x16x32_bf16 v[104:107], v[120:123], v[208:211], v[104:107]
	global_load_dwordx4 v[108:111], v[52:53], off offset:256
	global_load_dwordx4 v[120:123], v[54:55], off offset:256
	global_load_dwordx4 v[200:203], v[56:57], off offset:256
	global_load_dwordx4 v[204:207], v[58:59], off offset:256
	global_load_dwordx4 v[212:215], v[60:61], off offset:256
	s_waitcnt vmcnt(11)
	ds_write_b128 v79, v[16:19] offset:64512
	s_waitcnt vmcnt(10)
	ds_write_b128 v80, v[20:23]
	s_waitcnt vmcnt(9)
	ds_write_b128 v81, v[32:35]
	v_mfma_f32_16x16x32_bf16 v[4:7], v[196:199], v[208:211], v[4:7]
	v_mfma_f32_16x16x32_bf16 v[0:3], v[216:219], v[208:211], v[0:3]
	s_waitcnt lgkmcnt(0)
	s_barrier
	ds_read_b64_tr_b16 v[16:17], v77
	ds_read_b64_tr_b16 v[18:19], v78
	ds_read_b128 v[12:15], v62 offset:46080
	ds_read_b64_tr_b16 v[20:21], v74
	ds_read_b64_tr_b16 v[22:23], v75
	ds_read_b64_tr_b16 v[196:197], v76
	ds_read_b128 v[32:35], v62 offset:48384
	ds_read_b128 v[208:211], v62 offset:55296
	ds_read_b64_tr_b16 v[198:199], v71
	ds_read_b64_tr_b16 v[216:217], v72
	ds_read_b64_tr_b16 v[218:219], v73
	s_waitcnt lgkmcnt(8)
	v_mfma_f32_16x16x32_bf16 v[116:119], v[16:19], v[12:15], v[116:119]
	ds_read_b128 v[220:223], v62 offset:50688
	s_waitcnt vmcnt(8)
	v_cvt_pk_bf16_f32 v48, v48, v49
	v_cvt_pk_bf16_f32 v49, v50, v51
	s_waitcnt lgkmcnt(7)
	v_mfma_f32_16x16x32_bf16 v[124:127], v[20:23], v[12:15], v[124:127]
	s_waitcnt vmcnt(7)
	v_cvt_pk_bf16_f32 v44, v44, v45
	v_cvt_pk_bf16_f32 v45, v46, v47
	s_waitcnt lgkmcnt(3)
	v_mfma_f32_16x16x32_bf16 v[128:131], v[196:199], v[12:15], v[128:131]
	s_waitcnt lgkmcnt(1)
	v_mfma_f32_16x16x32_bf16 v[152:155], v[216:219], v[12:15], v[152:155]
	v_lshl_add_u64 v[12:13], s[8:9], 0, v[146:147]
	v_lshl_add_u64 v[12:13], v[12:13], 0, s[10:11]
	v_lshl_add_u64 v[12:13], v[12:13], 0, v[132:133]
	v_lshl_add_u64 v[12:13], v[12:13], 0, v[148:149]
	v_lshl_add_u64 v[12:13], v[12:13], 0, v[150:151]
	v_add_co_u32_e32 v14, vcc, s18, v12
	v_mfma_f32_16x16x32_bf16 v[164:167], v[16:19], v[32:35], v[164:167]
	s_nop 0
	v_addc_co_u32_e32 v15, vcc, 0, v13, vcc
	global_load_dwordx4 v[224:227], v[12:13], off
	global_load_dwordx4 v[228:231], v[14:15], off
	v_add_co_u32_e32 v14, vcc, s19, v12
	v_mfma_f32_16x16x32_bf16 v[168:171], v[20:23], v[32:35], v[168:171]
	s_nop 0
	v_addc_co_u32_e32 v15, vcc, 0, v13, vcc
	v_add_co_u32_e32 v12, vcc, s20, v12
	v_mfma_f32_16x16x32_bf16 v[172:175], v[196:199], v[32:35], v[172:175]
	s_nop 0
	v_addc_co_u32_e32 v13, vcc, 0, v13, vcc
	ds_read_b128 v[232:235], v62 offset:52992
	v_mfma_f32_16x16x32_bf16 v[112:115], v[216:219], v[32:35], v[112:115]
	global_load_dwordx4 v[32:35], v[14:15], off
	s_nop 0
	global_load_dwordx4 v[12:15], v[12:13], off
	ds_write_b64 v238, v[48:49]
	ds_write_b64 v239, v[44:45]
	s_waitcnt lgkmcnt(3)
	v_mfma_f32_16x16x32_bf16 v[24:27], v[216:219], v[220:223], v[24:27]
	v_mfma_f32_16x16x32_bf16 v[184:187], v[16:19], v[220:223], v[184:187]
	v_mfma_f32_16x16x32_bf16 v[188:191], v[20:23], v[220:223], v[188:191]
	v_mfma_f32_16x16x32_bf16 v[192:195], v[196:199], v[220:223], v[192:195]
	s_waitcnt lgkmcnt(2)
	v_mfma_f32_16x16x32_bf16 v[8:11], v[16:19], v[232:235], v[8:11]
	v_mfma_f32_16x16x32_bf16 v[28:31], v[20:23], v[232:235], v[28:31]
	v_mfma_f32_16x16x32_bf16 v[44:47], v[196:199], v[232:235], v[176:179]
	v_mfma_f32_16x16x32_bf16 v[16:19], v[16:19], v[208:211], v[100:103]
	s_nop 2
	ds_read_b128 v[100:103], v62 offset:46144
	ds_read_b128 v[176:179], v62 offset:48448
	v_mfma_f32_16x16x32_bf16 v[20:23], v[20:23], v[208:211], v[104:107]
	s_nop 2
	ds_read_b128 v[104:107], v62 offset:50752
	v_mfma_f32_16x16x32_bf16 v[48:51], v[216:219], v[232:235], v[180:183]
	s_waitcnt vmcnt(10)
	s_nop 1
	v_cvt_pk_bf16_f32 v180, v40, v41
	v_cvt_pk_bf16_f32 v181, v42, v43
	v_mfma_f32_16x16x32_bf16 v[40:43], v[196:199], v[208:211], v[4:7]
	ds_write_b64 v240, v[180:181]
	s_waitcnt vmcnt(9)
	s_nop 0
	v_cvt_pk_bf16_f32 v4, v36, v37
	v_cvt_pk_bf16_f32 v5, v38, v39
	v_mfma_f32_16x16x32_bf16 v[36:39], v[216:219], v[208:211], v[0:3]
	ds_write_b64 v241, v[4:5]
	s_nop 1
	ds_read_b64_tr_b16 v[0:1], v68
	ds_read_b64_tr_b16 v[2:3], v70
	ds_read_b64_tr_b16 v[4:5], v67
	ds_read_b64_tr_b16 v[6:7], v69
	ds_read_b64_tr_b16 v[180:181], v63
	ds_read_b64_tr_b16 v[182:183], v64
	ds_read_b64_tr_b16 v[196:197], v65
	ds_read_b64_tr_b16 v[198:199], v66
	s_waitcnt lgkmcnt(6)
	v_mfma_f32_16x16x32_bf16 v[116:119], v[0:3], v[100:103], v[116:119]
	s_waitcnt lgkmcnt(4)
	v_mfma_f32_16x16x32_bf16 v[124:127], v[4:7], v[100:103], v[124:127]
	s_waitcnt lgkmcnt(2)
	v_mfma_f32_16x16x32_bf16 v[128:131], v[180:183], v[100:103], v[128:131]
	s_waitcnt lgkmcnt(0)
	v_mfma_f32_16x16x32_bf16 v[100:103], v[196:199], v[100:103], v[152:155]
	v_mfma_f32_16x16x32_bf16 v[152:155], v[0:3], v[176:179], v[164:167]
	v_mfma_f32_16x16x32_bf16 v[164:167], v[4:7], v[176:179], v[168:171]
	v_mfma_f32_16x16x32_bf16 v[168:171], v[180:183], v[176:179], v[172:175]
	v_mfma_f32_16x16x32_bf16 v[112:115], v[196:199], v[176:179], v[112:115]
	v_mfma_f32_16x16x32_bf16 v[172:175], v[0:3], v[104:107], v[184:187]
	v_mfma_f32_16x16x32_bf16 v[176:179], v[4:7], v[104:107], v[188:191]
	v_mfma_f32_16x16x32_bf16 v[184:187], v[180:183], v[104:107], v[192:195]
	s_nop 1
	ds_read_b128 v[188:191], v62 offset:53056
	ds_read_b128 v[192:195], v62 offset:55360
	s_waitcnt vmcnt(8)
	ds_write_b128 v79, v[108:111]
	s_waitcnt vmcnt(7)
	ds_write_b128 v79, v[120:123] offset:9216
	v_mfma_f32_16x16x32_bf16 v[104:107], v[196:199], v[104:107], v[24:27]
	s_waitcnt lgkmcnt(3)
	v_mfma_f32_16x16x32_bf16 v[108:111], v[0:3], v[188:191], v[8:11]
	v_mfma_f32_16x16x32_bf16 v[120:123], v[4:7], v[188:191], v[28:31]
	v_mfma_f32_16x16x32_bf16 v[44:47], v[180:183], v[188:191], v[44:47]
	v_mfma_f32_16x16x32_bf16 v[48:51], v[196:199], v[188:191], v[48:51]
	s_waitcnt lgkmcnt(2)
	v_mfma_f32_16x16x32_bf16 v[188:191], v[0:3], v[192:195], v[16:19]
	v_mfma_f32_16x16x32_bf16 v[208:211], v[4:7], v[192:195], v[20:23]
	global_load_dwordx4 v[216:219], v[52:53], off offset:384
	s_nop 0
	global_load_dwordx4 v[52:55], v[54:55], off offset:384
	s_nop 0
	global_load_dwordx4 v[0:3], v[56:57], off offset:384
	global_load_dwordx4 v[4:7], v[58:59], off offset:384
	global_load_dwordx4 v[8:11], v[60:61], off offset:384
	s_waitcnt vmcnt(11)
	ds_write_b128 v79, v[200:203] offset:18432
	s_waitcnt vmcnt(10)
	ds_write_b128 v79, v[204:207] offset:27648
	s_waitcnt vmcnt(9)
	ds_write_b128 v79, v[212:215] offset:36864
	v_mfma_f32_16x16x32_bf16 v[40:43], v[180:183], v[192:195], v[40:43]
	v_mfma_f32_16x16x32_bf16 v[36:39], v[196:199], v[192:195], v[36:39]
	s_cmpk_lt_i32 s26, 0x100
	s_cselect_b32 s8, s26, 1
	s_waitcnt lgkmcnt(0)
	s_barrier
	ds_read_b64_tr_b16 v[56:57], v84
	ds_read_b64_tr_b16 v[58:59], v85
	ds_read_b64_tr_b16 v[84:85], v86
	ds_read_b64_tr_b16 v[86:87], v87
	ds_read_b128 v[16:19], v62
	ds_read_b64_tr_b16 v[180:181], v82
	ds_read_b64_tr_b16 v[182:183], v83
	ds_read_b128 v[20:23], v62 offset:2304
	ds_read_b64_tr_b16 v[192:193], v236
	ds_read_b64_tr_b16 v[194:195], v237
	s_cselect_b32 s10, s17, s49
	s_cselect_b32 s11, s16, s48
	s_ashr_i32 s9, s8, 31
	s_lshl_b64 s[8:9], s[8:9], 20
	s_add_u32 s8, s11, s8
	s_addc_u32 s9, s10, s9
	s_lshl_b32 s10, s27, 7
	s_ashr_i32 s11, s10, 31
	s_waitcnt lgkmcnt(5)
	v_mfma_f32_16x16x32_bf16 v[116:119], v[56:59], v[16:19], v[116:119]
	s_lshl_b64 s[10:11], s[10:11], 2
	ds_read_b128 v[196:199], v62 offset:4608
	s_waitcnt vmcnt(8)
	v_cvt_pk_bf16_f32 v60, v224, v225
	v_mfma_f32_16x16x32_bf16 v[124:127], v[84:87], v[16:19], v[124:127]
	v_cvt_pk_bf16_f32 v61, v226, v227
	s_waitcnt lgkmcnt(4)
	v_mfma_f32_16x16x32_bf16 v[128:131], v[180:183], v[16:19], v[128:131]
	s_waitcnt lgkmcnt(1)
	v_mfma_f32_16x16x32_bf16 v[100:103], v[192:195], v[16:19], v[100:103]
	v_lshl_add_u64 v[16:17], s[8:9], 0, v[136:137]
	v_lshl_add_u64 v[16:17], v[16:17], 0, s[10:11]
	v_lshl_add_u64 v[16:17], v[16:17], 0, v[132:133]
	v_lshl_add_u64 v[16:17], v[16:17], 0, v[148:149]
	v_lshl_add_u64 v[24:25], v[16:17], 0, v[150:151]
	v_add_co_u32_e32 v16, vcc, s18, v24
	v_mfma_f32_16x16x32_bf16 v[152:155], v[56:59], v[20:23], v[152:155]
	s_nop 0
	v_addc_co_u32_e32 v17, vcc, 0, v25, vcc
	v_add_co_u32_e32 v26, vcc, s19, v24
	v_mfma_f32_16x16x32_bf16 v[164:167], v[84:87], v[20:23], v[164:167]
	s_nop 0
	v_addc_co_u32_e32 v27, vcc, 0, v25, vcc
	v_mfma_f32_16x16x32_bf16 v[168:171], v[180:183], v[20:23], v[168:171]
	v_mfma_f32_16x16x32_bf16 v[112:115], v[192:195], v[20:23], v[112:115]
	global_load_dwordx4 v[20:23], v[24:25], off
	s_nop 0
	global_load_dwordx4 v[16:19], v[16:17], off
	v_add_co_u32_e32 v24, vcc, s20, v24
	ds_read_b128 v[200:203], v62 offset:6912
	s_nop 0
	v_addc_co_u32_e32 v25, vcc, 0, v25, vcc
	global_load_dwordx4 v[28:31], v[26:27], off
	s_nop 0
	global_load_dwordx4 v[24:27], v[24:25], off
	ds_read_b128 v[204:207], v62 offset:9216
	s_waitcnt lgkmcnt(2)
	v_mfma_f32_16x16x32_bf16 v[104:107], v[192:195], v[196:199], v[104:107]
	ds_write_b64 v99, v[60:61]
	s_waitcnt vmcnt(11)
	v_cvt_pk_bf16_f32 v60, v228, v229
	v_cvt_pk_bf16_f32 v61, v230, v231
	v_mfma_f32_16x16x32_bf16 v[172:175], v[56:59], v[196:199], v[172:175]
	ds_write_b64 v98, v[60:61]
	v_mfma_f32_16x16x32_bf16 v[176:179], v[84:87], v[196:199], v[176:179]
	v_mfma_f32_16x16x32_bf16 v[184:187], v[180:183], v[196:199], v[184:187]
	s_waitcnt lgkmcnt(3)
	v_mfma_f32_16x16x32_bf16 v[108:111], v[56:59], v[200:203], v[108:111]
	s_waitcnt vmcnt(9)
	v_cvt_pk_bf16_f32 v12, v12, v13
	v_cvt_pk_bf16_f32 v13, v14, v15
	v_cvt_pk_bf16_f32 v32, v32, v33
	s_waitcnt lgkmcnt(2)
	v_mfma_f32_16x16x32_bf16 v[56:59], v[56:59], v[204:207], v[188:191]
	s_nop 2
	ds_read_b128 v[188:191], v62 offset:64
	ds_read_b128 v[196:199], v62 offset:2368
	v_cvt_pk_bf16_f32 v33, v34, v35
	v_mfma_f32_16x16x32_bf16 v[120:123], v[84:87], v[200:203], v[120:123]
	v_mfma_f32_16x16x32_bf16 v[44:47], v[180:183], v[200:203], v[44:47]
	v_mfma_f32_16x16x32_bf16 v[48:51], v[192:195], v[200:203], v[48:51]
	ds_read_b128 v[200:203], v62 offset:4672
	ds_write_b64 v92, v[12:13]
	ds_write_b64 v95, v[32:33]
	v_mfma_f32_16x16x32_bf16 v[82:85], v[84:87], v[204:207], v[208:211]
	v_mfma_f32_16x16x32_bf16 v[40:43], v[180:183], v[204:207], v[40:43]
	v_mfma_f32_16x16x32_bf16 v[12:15], v[192:195], v[204:207], v[36:39]
	ds_read_b64_tr_b16 v[32:33], v91
	ds_read_b64_tr_b16 v[34:35], v93
	ds_read_b64_tr_b16 v[180:181], v89
	ds_read_b64_tr_b16 v[182:183], v90
	ds_read_b64_tr_b16 v[86:87], v88
	ds_read_b64_tr_b16 v[88:89], v94
	ds_read_b64_tr_b16 v[94:95], v96
	ds_read_b64_tr_b16 v[96:97], v97
	s_waitcnt lgkmcnt(6)
	v_mfma_f32_16x16x32_bf16 v[90:93], v[32:35], v[188:191], v[116:119]
	s_waitcnt lgkmcnt(4)
	v_mfma_f32_16x16x32_bf16 v[116:119], v[180:183], v[188:191], v[124:127]
	s_waitcnt lgkmcnt(2)
	v_mfma_f32_16x16x32_bf16 v[124:127], v[86:89], v[188:191], v[128:131]
	v_mfma_f32_16x16x32_bf16 v[128:131], v[32:35], v[196:199], v[152:155]
	v_mfma_f32_16x16x32_bf16 v[152:155], v[180:183], v[196:199], v[164:167]
	v_mfma_f32_16x16x32_bf16 v[164:167], v[86:89], v[196:199], v[168:171]
	v_mfma_f32_16x16x32_bf16 v[168:171], v[32:35], v[200:203], v[172:175]
	v_mfma_f32_16x16x32_bf16 v[172:175], v[180:183], v[200:203], v[176:179]
	v_mfma_f32_16x16x32_bf16 v[176:179], v[86:89], v[200:203], v[184:187]
	ds_read_b128 v[36:39], v62 offset:6976
	s_nop 1
	ds_read_b128 v[184:187], v62 offset:9280
	s_waitcnt vmcnt(8)
	ds_write_b128 v79, v[216:219] offset:46080
	s_waitcnt vmcnt(7)
	ds_write_b128 v79, v[52:55] offset:55296
	s_waitcnt lgkmcnt(4)
	v_mfma_f32_16x16x32_bf16 v[98:101], v[94:97], v[188:191], v[100:103]
	v_mfma_f32_16x16x32_bf16 v[112:115], v[94:97], v[196:199], v[112:115]
	v_mfma_f32_16x16x32_bf16 v[52:55], v[94:97], v[200:203], v[104:107]
	v_sub_u32_e32 v60, v163, v143
	v_xad_u32 v192, s28, -1, v60
	v_add_u32_e32 v61, s28, v162
	s_waitcnt lgkmcnt(3)
	v_mfma_f32_16x16x32_bf16 v[102:105], v[32:35], v[36:39], v[108:111]
	v_min_i32_e32 v60, 0, v192
	s_nop 1
	v_add_u32_e32 v110, v61, v143
	v_mfma_f32_16x16x32_bf16 v[106:109], v[180:183], v[36:39], v[120:123]
	v_add_u32_e32 v60, v60, v110
	v_ashrrev_i32_e32 v61, 31, v60
	v_lshlrev_b64 v[60:61], 9, v[60:61]
	v_mfma_f32_16x16x32_bf16 v[120:123], v[86:89], v[36:39], v[44:47]
	s_nop 2
	v_min_i32_e32 v46, 64, v192
	v_add_u32_e32 v46, v46, v110
	v_ashrrev_i32_e32 v47, 31, v46
	v_lshl_add_u64 v[44:45], v[134:135], 0, v[60:61]
	v_mfma_f32_16x16x32_bf16 v[188:191], v[94:97], v[36:39], v[48:51]
	v_lshlrev_b64 v[36:37], 9, v[46:47]
	v_lshl_add_u64 v[46:47], v[134:135], 0, v[36:37]
	s_waitcnt lgkmcnt(2)
	v_mfma_f32_16x16x32_bf16 v[56:59], v[32:35], v[184:187], v[56:59]
	global_load_dwordx4 v[36:39], v[44:45], off
	global_load_dwordx4 v[32:35], v[46:47], off
	v_min_i32_e32 v44, 0x80, v192
	v_min_i32_e32 v48, 0x100, v192
	v_mfma_f32_16x16x32_bf16 v[86:89], v[86:89], v[184:187], v[40:43]
	v_add_u32_e32 v44, v44, v110
	v_add_u32_e32 v48, v48, v110
	v_ashrrev_i32_e32 v45, 31, v44
	v_min_i32_e32 v42, 0xc0, v192
	v_add_u32_e32 v42, v42, v110
	v_ashrrev_i32_e32 v43, 31, v42
	v_ashrrev_i32_e32 v49, 31, v48
	v_lshlrev_b64 v[44:45], 9, v[44:45]
	v_lshlrev_b64 v[42:43], 9, v[42:43]
	v_lshlrev_b64 v[48:49], 9, v[48:49]
	v_lshl_add_u64 v[40:41], v[134:135], 0, v[44:45]
	v_lshl_add_u64 v[42:43], v[134:135], 0, v[42:43]
	v_lshl_add_u64 v[48:49], v[134:135], 0, v[48:49]
	global_load_dwordx4 v[44:47], v[40:41], off
	s_nop 0
	global_load_dwordx4 v[40:43], v[42:43], off
	v_mfma_f32_16x16x32_bf16 v[82:85], v[180:183], v[184:187], v[82:85]
	global_load_dwordx4 v[48:51], v[48:49], off
	s_waitcnt vmcnt(11)
	ds_write_b128 v79, v[0:3] offset:64512
	s_waitcnt vmcnt(10)
	ds_write_b128 v80, v[4:7]
	s_waitcnt vmcnt(9)
	ds_write_b128 v81, v[8:11]
	v_mfma_f32_16x16x32_bf16 v[94:97], v[94:97], v[184:187], v[12:15]
	s_waitcnt lgkmcnt(0)
	s_barrier
	ds_read_b64_tr_b16 v[180:181], v77
	ds_read_b64_tr_b16 v[182:183], v78
	ds_read_b128 v[0:3], v62 offset:46080
	ds_read_b64_tr_b16 v[78:79], v74
	ds_read_b64_tr_b16 v[80:81], v75
	ds_read_b64_tr_b16 v[74:75], v76
	ds_read_b128 v[4:7], v62 offset:48384
	ds_read_b128 v[184:187], v62 offset:55296
	ds_read_b64_tr_b16 v[76:77], v71
	ds_read_b64_tr_b16 v[192:193], v72
	ds_read_b64_tr_b16 v[194:195], v73
	s_waitcnt lgkmcnt(8)
	v_mfma_f32_16x16x32_bf16 v[90:93], v[180:183], v[0:3], v[90:93]
	s_waitcnt lgkmcnt(6)
	v_mfma_f32_16x16x32_bf16 v[116:119], v[78:81], v[0:3], v[116:119]
	s_waitcnt lgkmcnt(2)
	v_mfma_f32_16x16x32_bf16 v[196:199], v[74:77], v[0:3], v[124:127]
	s_waitcnt lgkmcnt(0)
	v_mfma_f32_16x16x32_bf16 v[98:101], v[192:195], v[0:3], v[98:101]
	v_lshl_add_u64 v[0:1], s[8:9], 0, v[138:139]
	v_lshl_add_u64 v[0:1], v[0:1], 0, s[10:11]
	v_lshl_add_u64 v[0:1], v[0:1], 0, v[132:133]
	v_lshl_add_u64 v[0:1], v[0:1], 0, v[148:149]
	v_lshl_add_u64 v[0:1], v[0:1], 0, v[150:151]
	v_add_co_u32_e32 v2, vcc, s18, v0
	ds_read_b128 v[124:127], v62 offset:50688
	s_nop 0
	v_addc_co_u32_e32 v3, vcc, 0, v1, vcc
	global_load_dwordx4 v[12:15], v[0:1], off
	global_load_dwordx4 v[8:11], v[2:3], off
	v_add_co_u32_e32 v2, vcc, s19, v0
	v_mfma_f32_16x16x32_bf16 v[200:203], v[180:183], v[4:7], v[128:131]
	s_nop 0
	v_addc_co_u32_e32 v3, vcc, 0, v1, vcc
	v_add_co_u32_e32 v0, vcc, s20, v0
	v_mfma_f32_16x16x32_bf16 v[152:155], v[78:81], v[4:7], v[152:155]
	s_nop 0
	v_addc_co_u32_e32 v1, vcc, 0, v1, vcc
	v_mfma_f32_16x16x32_bf16 v[164:167], v[74:77], v[4:7], v[164:167]
	v_mfma_f32_16x16x32_bf16 v[204:207], v[192:195], v[4:7], v[112:115]
	s_nop 2
	ds_read_b128 v[110:113], v62 offset:52992
	global_load_dwordx4 v[4:7], v[2:3], off
	s_nop 0
	global_load_dwordx4 v[0:3], v[0:1], off
	s_waitcnt lgkmcnt(1)
	v_mfma_f32_16x16x32_bf16 v[52:55], v[192:195], v[124:127], v[52:55]
	v_mfma_f32_16x16x32_bf16 v[168:171], v[180:183], v[124:127], v[168:171]
	v_mfma_f32_16x16x32_bf16 v[172:175], v[78:81], v[124:127], v[172:175]
	v_mfma_f32_16x16x32_bf16 v[176:179], v[74:77], v[124:127], v[176:179]
	s_waitcnt lgkmcnt(0)
	v_mfma_f32_16x16x32_bf16 v[208:211], v[180:183], v[110:113], v[102:105]
	v_mfma_f32_16x16x32_bf16 v[212:215], v[78:81], v[110:113], v[106:109]
	v_mfma_f32_16x16x32_bf16 v[216:219], v[74:77], v[110:113], v[120:123]
	v_mfma_f32_16x16x32_bf16 v[56:59], v[180:183], v[184:187], v[56:59]
	v_mfma_f32_16x16x32_bf16 v[180:183], v[78:81], v[184:187], v[82:85]
	v_mfma_f32_16x16x32_bf16 v[220:223], v[74:77], v[184:187], v[86:89]
	ds_read_b128 v[72:75], v62 offset:46144
	ds_read_b128 v[76:79], v62 offset:48448
	ds_read_b128 v[80:83], v62 offset:50752
	v_mfma_f32_16x16x32_bf16 v[188:191], v[192:195], v[110:113], v[188:191]
	v_mfma_f32_16x16x32_bf16 v[184:187], v[192:195], v[184:187], v[94:97]
	ds_read_b64_tr_b16 v[192:193], v68
	ds_read_b64_tr_b16 v[194:195], v70
	ds_read_b64_tr_b16 v[224:225], v67
	ds_read_b64_tr_b16 v[226:227], v69
	ds_read_b64_tr_b16 v[228:229], v63
	ds_read_b64_tr_b16 v[230:231], v64
	ds_read_b64_tr_b16 v[232:233], v65
	ds_read_b64_tr_b16 v[234:235], v66
	s_waitcnt lgkmcnt(6)
	v_mfma_f32_16x16x32_bf16 v[124:127], v[192:195], v[72:75], v[90:93]
	s_waitcnt lgkmcnt(4)
	v_mfma_f32_16x16x32_bf16 v[108:111], v[224:227], v[76:79], v[152:155]
	ds_read_b128 v[64:67], v62 offset:53056
	s_nop 1
	ds_read_b128 v[152:155], v62 offset:55360
	v_mfma_f32_16x16x32_bf16 v[128:131], v[224:227], v[72:75], v[116:119]
	s_waitcnt lgkmcnt(4)
	v_mfma_f32_16x16x32_bf16 v[120:123], v[228:231], v[72:75], v[196:199]
	s_waitcnt lgkmcnt(2)
	v_mfma_f32_16x16x32_bf16 v[116:119], v[232:235], v[72:75], v[98:101]
	v_mfma_f32_16x16x32_bf16 v[112:115], v[192:195], v[76:79], v[200:203]
	v_mfma_f32_16x16x32_bf16 v[104:107], v[228:231], v[76:79], v[164:167]
	v_mfma_f32_16x16x32_bf16 v[100:103], v[232:235], v[76:79], v[204:207]
	v_mfma_f32_16x16x32_bf16 v[96:99], v[192:195], v[80:83], v[168:171]
	v_mfma_f32_16x16x32_bf16 v[92:95], v[224:227], v[80:83], v[172:175]
	v_mfma_f32_16x16x32_bf16 v[84:87], v[228:231], v[80:83], v[176:179]
	v_mfma_f32_16x16x32_bf16 v[88:91], v[232:235], v[80:83], v[52:55]
	s_waitcnt lgkmcnt(1)
	v_mfma_f32_16x16x32_bf16 v[80:83], v[192:195], v[64:67], v[208:211]
	v_mfma_f32_16x16x32_bf16 v[76:79], v[224:227], v[64:67], v[212:215]
	v_mfma_f32_16x16x32_bf16 v[72:75], v[228:231], v[64:67], v[216:219]
	v_mfma_f32_16x16x32_bf16 v[68:71], v[232:235], v[64:67], v[188:191]
	s_waitcnt lgkmcnt(0)
	v_mfma_f32_16x16x32_bf16 v[64:67], v[192:195], v[152:155], v[56:59]
	v_mfma_f32_16x16x32_bf16 v[60:63], v[224:227], v[152:155], v[180:183]
	v_mfma_f32_16x16x32_bf16 v[56:59], v[228:231], v[152:155], v[220:223]
	v_mfma_f32_16x16x32_bf16 v[52:55], v[232:235], v[152:155], v[184:187]
	v_add_u32_e32 v149, s14, v157
	v_cmp_lt_i32_e32 vcc, v149, v156
	v_lshlrev_b32_e32 v154, 1, v140
	v_lshlrev_b32_e32 v152, 1, v142
	s_and_saveexec_b64 s[8:9], vcc
	s_cbranch_execz .LBB0_2487
	v_add_u32_e32 v164, v141, v149
	v_ashrrev_i32_e32 v165, 31, v164
	v_readlane_b32 s10, v254, 3
	v_lshlrev_b64 v[164:165], 11, v[164:165]
	v_readlane_b32 s11, v254, 4
	v_mov_b32_e32 v155, v133
	v_mov_b32_e32 v153, v133
	v_lshl_add_u64 v[164:165], s[10:11], 0, v[164:165]
	v_lshl_add_u64 v[164:165], s[6:7], 1, v[164:165]
	v_lshl_add_u64 v[164:165], v[164:165], 0, v[154:155]
	v_lshl_add_u64 v[164:165], v[164:165], 0, v[152:153]
	v_cvt_pk_bf16_f32 v124, v124, v125
	v_cvt_pk_bf16_f32 v125, v126, v127
	v_cvt_pk_bf16_f32 v126, v128, v129
	v_cvt_pk_bf16_f32 v127, v130, v131
	v_cvt_pk_bf16_f32 v120, v120, v121
	v_cvt_pk_bf16_f32 v121, v122, v123
	v_cvt_pk_bf16_f32 v122, v116, v117
	v_cvt_pk_bf16_f32 v123, v118, v119
	global_store_dwordx4 v[164:165], v[124:127], off nt
	global_store_dwordx4 v[164:165], v[120:123], off offset:16 nt
.LBB0_2487:
	s_or_b64 exec, exec, s[8:9]
	v_add_u32_e32 v116, s14, v158
	v_cmp_lt_i32_e32 vcc, v116, v156
	s_and_saveexec_b64 s[8:9], vcc
	s_cbranch_execz .LBB0_2489
	v_add_u32_e32 v116, v141, v116
	v_ashrrev_i32_e32 v117, 31, v116
	v_readlane_b32 s10, v254, 3
	v_lshlrev_b64 v[116:117], 11, v[116:117]
	v_readlane_b32 s11, v254, 4
	v_mov_b32_e32 v155, v133
	v_mov_b32_e32 v153, v133
	v_lshl_add_u64 v[116:117], s[10:11], 0, v[116:117]
	v_lshl_add_u64 v[116:117], s[6:7], 1, v[116:117]
	v_lshl_add_u64 v[116:117], v[116:117], 0, v[154:155]
	v_lshl_add_u64 v[116:117], v[116:117], 0, v[152:153]
	v_cvt_pk_bf16_f32 v112, v112, v113
	v_cvt_pk_bf16_f32 v113, v114, v115
	v_cvt_pk_bf16_f32 v114, v108, v109
	v_cvt_pk_bf16_f32 v115, v110, v111
	v_cvt_pk_bf16_f32 v104, v104, v105
	v_cvt_pk_bf16_f32 v105, v106, v107
	v_cvt_pk_bf16_f32 v106, v100, v101
	v_cvt_pk_bf16_f32 v107, v102, v103
	global_store_dwordx4 v[116:117], v[112:115], off nt
	global_store_dwordx4 v[116:117], v[104:107], off offset:16 nt
